# v2 + s_setprio 3 around MFMA blocks (repeat)
# speedup vs baseline: 1.0052x; 1.0052x over previous
.LBB0_171:
	s_add_u32 s16, s62, 0x4000
	s_addc_u32 s17, s63, 0
	s_cmp_eq_u32 vcc_hi, 28
	s_cselect_b32 s68, s29, s16
	s_cselect_b32 s69, s15, s17
	s_cselect_b32 s67, s53, vcc_lo
	s_cselect_b32 s66, s55, s61
	s_add_u32 s64, s68, 0x8000
	s_addc_u32 s65, s69, 0
	s_add_i32 s16, 0, 0x10000
	s_add_i32 s17, 0, 0x14000
	v_add_u32_e32 v94, s16, v182
	v_add_u32_e32 v114, s17, v182
	ds_read_b128 v[82:85], v94
	ds_read_b128 v[86:89], v94 offset:1024
	ds_read_b128 v[90:93], v94 offset:2048
	ds_read_b128 v[94:97], v94 offset:3072
	ds_read_b128 v[174:177], v114
	ds_read_b128 v[178:181], v114 offset:1024
	ds_read_b128 v[214:217], v114 offset:2048
	ds_read_b128 v[218:221], v114 offset:3072
	v_lshl_add_u64 v[158:159], s[62:63], 0, v[170:171]
	s_add_i32 m0, s37, 0xc000
	ds_read_b128 v[222:225], v212
	ds_read_b128 v[226:229], v212 offset:1024
	ds_read_b128 v[230:233], v212 offset:2048
	ds_read_b128 v[234:237], v212 offset:3072
	ds_read_b128 v[238:241], v212 offset:4096
	ds_read_b128 v[242:245], v212 offset:5120
	ds_read_b128 v[246:249], v212 offset:6144
	ds_read_b128 v[250:253], v212 offset:7168
	global_load_lds_dwordx4 v[158:159], off
	v_lshl_add_u64 v[158:159], s[62:63], 0, v[172:173]
	s_add_i32 m0, s37, 0xe000
	s_nop 0
	global_load_lds_dwordx4 v[158:159], off
	s_waitcnt vmcnt(8)
	s_waitcnt lgkmcnt(0)
	s_barrier
	s_setprio 3
	s_waitcnt lgkmcnt(0)
	v_mfma_f32_16x16x32_bf16 v[144:147], v[82:85], v[222:225], v[144:147]
	v_mfma_f32_16x16x32_bf16 v[140:143], v[90:93], v[222:225], v[140:143]
	v_mfma_f32_16x16x32_bf16 v[128:131], v[82:85], v[230:233], v[128:131]
	v_mfma_f32_16x16x32_bf16 v[124:127], v[90:93], v[230:233], v[124:127]
	v_mfma_f32_16x16x32_bf16 v[110:113], v[82:85], v[238:241], v[110:113]
	v_mfma_f32_16x16x32_bf16 v[106:109], v[90:93], v[238:241], v[106:109]
	v_mfma_f32_16x16x32_bf16 v[78:81], v[82:85], v[246:249], v[78:81]
	v_mfma_f32_16x16x32_bf16 v[74:77], v[90:93], v[246:249], v[74:77]
	v_mfma_f32_16x16x32_bf16 v[144:147], v[86:89], v[226:229], v[144:147]
	v_mfma_f32_16x16x32_bf16 v[140:143], v[94:97], v[226:229], v[140:143]
	v_mfma_f32_16x16x32_bf16 v[128:131], v[86:89], v[234:237], v[128:131]
	v_mfma_f32_16x16x32_bf16 v[124:127], v[94:97], v[234:237], v[124:127]
	v_mfma_f32_16x16x32_bf16 v[110:113], v[86:89], v[242:245], v[110:113]
	v_mfma_f32_16x16x32_bf16 v[106:109], v[94:97], v[242:245], v[106:109]
	v_mfma_f32_16x16x32_bf16 v[78:81], v[86:89], v[250:253], v[78:81]
	v_mfma_f32_16x16x32_bf16 v[74:77], v[94:97], v[250:253], v[74:77]
	s_setprio 0
	s_setprio 3
	v_mfma_f32_16x16x32_bf16 v[136:139], v[174:177], v[222:225], v[136:139]
	v_mfma_f32_16x16x32_bf16 v[132:135], v[214:217], v[222:225], v[132:135]
	v_mfma_f32_16x16x32_bf16 v[120:123], v[174:177], v[230:233], v[120:123]
	v_mfma_f32_16x16x32_bf16 v[116:119], v[214:217], v[230:233], v[116:119]
	v_mfma_f32_16x16x32_bf16 v[102:105], v[174:177], v[238:241], v[102:105]
	v_mfma_f32_16x16x32_bf16 v[98:101], v[214:217], v[238:241], v[98:101]
	v_mfma_f32_16x16x32_bf16 v[70:73], v[174:177], v[246:249], v[70:73]
	v_mfma_f32_16x16x32_bf16 v[66:69], v[214:217], v[246:249], v[66:69]
	v_mfma_f32_16x16x32_bf16 v[136:139], v[178:181], v[226:229], v[136:139]
	v_mfma_f32_16x16x32_bf16 v[132:135], v[218:221], v[226:229], v[132:135]
	v_mfma_f32_16x16x32_bf16 v[120:123], v[178:181], v[234:237], v[120:123]
	v_mfma_f32_16x16x32_bf16 v[116:119], v[218:221], v[234:237], v[116:119]
	v_mfma_f32_16x16x32_bf16 v[102:105], v[178:181], v[242:245], v[102:105]
	v_mfma_f32_16x16x32_bf16 v[98:101], v[218:221], v[242:245], v[98:101]
	v_mfma_f32_16x16x32_bf16 v[70:73], v[178:181], v[250:253], v[70:73]
	v_mfma_f32_16x16x32_bf16 v[66:69], v[218:221], v[250:253], v[66:69]
	s_setprio 0
	s_barrier
	s_add_i32 s16, s16, s9
	v_lshl_add_u64 v[158:159], s[66:67], 0, v[150:151]
	s_mov_b32 m0, s16
	ds_read_b128 v[222:225], v212 offset:16384
	ds_read_b128 v[226:229], v212 offset:17408
	ds_read_b128 v[230:233], v212 offset:18432
	ds_read_b128 v[234:237], v212 offset:19456
	ds_read_b128 v[238:241], v212 offset:20480
	ds_read_b128 v[242:245], v212 offset:21504
	ds_read_b128 v[246:249], v212 offset:22528
	ds_read_b128 v[250:253], v212 offset:23552
	global_load_lds_dwordx4 v[158:159], off
	s_add_i32 m0, s16, 0x2000
	s_add_u32 s26, s66, 0x1000
	v_lshl_add_u64 v[158:159], s[66:67], 0, v[154:155]
	s_addc_u32 s27, s67, 0
	s_add_i32 s16, s17, s9
	global_load_lds_dwordx4 v[158:159], off
	v_lshl_add_u64 v[158:159], s[26:27], 0, v[150:151]
	s_mov_b32 m0, s16
	s_nop 0
	global_load_lds_dwordx4 v[158:159], off
	v_lshl_add_u64 v[158:159], s[26:27], 0, v[154:155]
	s_add_i32 m0, s16, 0x2000
	s_nop 0
	global_load_lds_dwordx4 v[158:159], off
	v_lshl_add_u64 v[158:159], s[68:69], 0, v[148:149]
	s_mov_b32 m0, s37
	s_nop 0
	global_load_lds_dwordx4 v[158:159], off
	v_lshl_add_u64 v[158:159], s[68:69], 0, v[152:153]
	s_mov_b32 m0, s70
	s_nop 0
	global_load_lds_dwordx4 v[158:159], off
	s_waitcnt vmcnt(8)
	s_waitcnt lgkmcnt(0)
	s_barrier
	s_setprio 3
	s_waitcnt lgkmcnt(0)
	v_mfma_f32_16x16x32_bf16 v[62:65], v[82:85], v[222:225], v[62:65]
	v_mfma_f32_16x16x32_bf16 v[58:61], v[90:93], v[222:225], v[58:61]
	v_mfma_f32_16x16x32_bf16 v[46:49], v[82:85], v[230:233], v[46:49]
	v_mfma_f32_16x16x32_bf16 v[42:45], v[90:93], v[230:233], v[42:45]
	v_mfma_f32_16x16x32_bf16 v[30:33], v[82:85], v[238:241], v[30:33]
	v_mfma_f32_16x16x32_bf16 v[26:29], v[90:93], v[238:241], v[26:29]
	v_mfma_f32_16x16x32_bf16 v[14:17], v[82:85], v[246:249], v[14:17]
	v_mfma_f32_16x16x32_bf16 v[10:13], v[90:93], v[246:249], v[10:13]
	v_mfma_f32_16x16x32_bf16 v[62:65], v[86:89], v[226:229], v[62:65]
	v_mfma_f32_16x16x32_bf16 v[58:61], v[94:97], v[226:229], v[58:61]
	v_mfma_f32_16x16x32_bf16 v[46:49], v[86:89], v[234:237], v[46:49]
	v_mfma_f32_16x16x32_bf16 v[42:45], v[94:97], v[234:237], v[42:45]
	v_mfma_f32_16x16x32_bf16 v[30:33], v[86:89], v[242:245], v[30:33]
	v_mfma_f32_16x16x32_bf16 v[26:29], v[94:97], v[242:245], v[26:29]
	v_mfma_f32_16x16x32_bf16 v[14:17], v[86:89], v[250:253], v[14:17]
	v_mfma_f32_16x16x32_bf16 v[10:13], v[94:97], v[250:253], v[10:13]
	s_setprio 0
	s_setprio 3
	v_mfma_f32_16x16x32_bf16 v[54:57], v[174:177], v[222:225], v[54:57]
	v_mfma_f32_16x16x32_bf16 v[50:53], v[214:217], v[222:225], v[50:53]
	v_mfma_f32_16x16x32_bf16 v[38:41], v[174:177], v[230:233], v[38:41]
	v_mfma_f32_16x16x32_bf16 v[34:37], v[214:217], v[230:233], v[34:37]
	v_mfma_f32_16x16x32_bf16 v[22:25], v[174:177], v[238:241], v[22:25]
	v_mfma_f32_16x16x32_bf16 v[18:21], v[214:217], v[238:241], v[18:21]
	v_mfma_f32_16x16x32_bf16 v[6:9], v[174:177], v[246:249], v[6:9]
	v_mfma_f32_16x16x32_bf16 v[2:5], v[214:217], v[246:249], v[2:5]
	v_mfma_f32_16x16x32_bf16 v[54:57], v[178:181], v[226:229], v[54:57]
	v_mfma_f32_16x16x32_bf16 v[50:53], v[218:221], v[226:229], v[50:53]
	v_mfma_f32_16x16x32_bf16 v[38:41], v[178:181], v[234:237], v[38:41]
	v_mfma_f32_16x16x32_bf16 v[34:37], v[218:221], v[234:237], v[34:37]
	v_mfma_f32_16x16x32_bf16 v[22:25], v[178:181], v[242:245], v[22:25]
	v_mfma_f32_16x16x32_bf16 v[18:21], v[218:221], v[242:245], v[18:21]
	v_mfma_f32_16x16x32_bf16 v[6:9], v[178:181], v[250:253], v[6:9]
	v_mfma_f32_16x16x32_bf16 v[2:5], v[218:221], v[250:253], v[2:5]
	s_setprio 0
	s_barrier
	s_add_i32 s16, 0, 0x18000
	s_add_i32 s17, 0, 0x1c000
	v_add_u32_e32 v94, s16, v182
	v_add_u32_e32 v114, s17, v182
	ds_read_b128 v[82:85], v94
	ds_read_b128 v[86:89], v94 offset:1024
	ds_read_b128 v[90:93], v94 offset:2048
	ds_read_b128 v[94:97], v94 offset:3072
	ds_read_b128 v[174:177], v114
	ds_read_b128 v[178:181], v114 offset:1024
	ds_read_b128 v[214:217], v114 offset:2048
	ds_read_b128 v[218:221], v114 offset:3072
	s_add_u32 s26, s68, 0x4000
	s_addc_u32 s27, s69, 0
	s_mov_b32 m0, s71
	v_lshl_add_u64 v[158:159], s[26:27], 0, v[148:149]
	ds_read_b128 v[222:225], v212 offset:32768
	ds_read_b128 v[226:229], v212 offset:33792
	ds_read_b128 v[230:233], v212 offset:34816
	ds_read_b128 v[234:237], v212 offset:35840
	ds_read_b128 v[238:241], v212 offset:36864
	ds_read_b128 v[242:245], v212 offset:37888
	ds_read_b128 v[246:249], v212 offset:38912
	ds_read_b128 v[250:253], v212 offset:39936
	global_load_lds_dwordx4 v[158:159], off
	v_lshl_add_u64 v[158:159], s[26:27], 0, v[152:153]
	s_mov_b32 m0, s74
	s_nop 0
	global_load_lds_dwordx4 v[158:159], off
	s_waitcnt vmcnt(8)
	s_waitcnt lgkmcnt(0)
	s_barrier
	s_setprio 3
	s_waitcnt lgkmcnt(0)
	v_mfma_f32_16x16x32_bf16 v[144:147], v[82:85], v[222:225], v[144:147]
	v_mfma_f32_16x16x32_bf16 v[140:143], v[90:93], v[222:225], v[140:143]
	v_mfma_f32_16x16x32_bf16 v[128:131], v[82:85], v[230:233], v[128:131]
	v_mfma_f32_16x16x32_bf16 v[124:127], v[90:93], v[230:233], v[124:127]
	v_mfma_f32_16x16x32_bf16 v[110:113], v[82:85], v[238:241], v[110:113]
	v_mfma_f32_16x16x32_bf16 v[106:109], v[90:93], v[238:241], v[106:109]
	v_mfma_f32_16x16x32_bf16 v[78:81], v[82:85], v[246:249], v[78:81]
	v_mfma_f32_16x16x32_bf16 v[74:77], v[90:93], v[246:249], v[74:77]
	v_mfma_f32_16x16x32_bf16 v[144:147], v[86:89], v[226:229], v[144:147]
	v_mfma_f32_16x16x32_bf16 v[140:143], v[94:97], v[226:229], v[140:143]
	v_mfma_f32_16x16x32_bf16 v[128:131], v[86:89], v[234:237], v[128:131]
	v_mfma_f32_16x16x32_bf16 v[124:127], v[94:97], v[234:237], v[124:127]
	v_mfma_f32_16x16x32_bf16 v[110:113], v[86:89], v[242:245], v[110:113]
	v_mfma_f32_16x16x32_bf16 v[106:109], v[94:97], v[242:245], v[106:109]
	v_mfma_f32_16x16x32_bf16 v[78:81], v[86:89], v[250:253], v[78:81]
	v_mfma_f32_16x16x32_bf16 v[74:77], v[94:97], v[250:253], v[74:77]
	s_setprio 0
	s_setprio 3
	v_mfma_f32_16x16x32_bf16 v[136:139], v[174:177], v[222:225], v[136:139]
	v_mfma_f32_16x16x32_bf16 v[132:135], v[214:217], v[222:225], v[132:135]
	v_mfma_f32_16x16x32_bf16 v[120:123], v[174:177], v[230:233], v[120:123]
	v_mfma_f32_16x16x32_bf16 v[116:119], v[214:217], v[230:233], v[116:119]
	v_mfma_f32_16x16x32_bf16 v[102:105], v[174:177], v[238:241], v[102:105]
	v_mfma_f32_16x16x32_bf16 v[98:101], v[214:217], v[238:241], v[98:101]
	v_mfma_f32_16x16x32_bf16 v[70:73], v[174:177], v[246:249], v[70:73]
	v_mfma_f32_16x16x32_bf16 v[66:69], v[214:217], v[246:249], v[66:69]
	v_mfma_f32_16x16x32_bf16 v[136:139], v[178:181], v[226:229], v[136:139]
	v_mfma_f32_16x16x32_bf16 v[132:135], v[218:221], v[226:229], v[132:135]
	v_mfma_f32_16x16x32_bf16 v[120:123], v[178:181], v[234:237], v[120:123]
	v_mfma_f32_16x16x32_bf16 v[116:119], v[218:221], v[234:237], v[116:119]
	v_mfma_f32_16x16x32_bf16 v[102:105], v[178:181], v[242:245], v[102:105]
	v_mfma_f32_16x16x32_bf16 v[98:101], v[218:221], v[242:245], v[98:101]
	v_mfma_f32_16x16x32_bf16 v[70:73], v[178:181], v[250:253], v[70:73]
	v_mfma_f32_16x16x32_bf16 v[66:69], v[218:221], v[250:253], v[66:69]
	s_setprio 0
	s_barrier
	s_add_u32 s26, s66, 0x8000
	s_addc_u32 s27, s67, 0
	s_add_i32 s16, s16, s9
	v_lshl_add_u64 v[158:159], s[26:27], 0, v[150:151]
	s_mov_b32 m0, s16
	ds_read_b128 v[222:225], v212 offset:49152
	ds_read_b128 v[226:229], v212 offset:50176
	ds_read_b128 v[230:233], v212 offset:51200
	ds_read_b128 v[234:237], v212 offset:52224
	ds_read_b128 v[238:241], v212 offset:53248
	ds_read_b128 v[242:245], v212 offset:54272
	ds_read_b128 v[246:249], v212 offset:55296
	ds_read_b128 v[250:253], v212 offset:56320
	global_load_lds_dwordx4 v[158:159], off
	s_add_i32 m0, s16, 0x2000
	v_lshl_add_u64 v[158:159], s[26:27], 0, v[154:155]
	s_add_u32 s26, s66, 0x9000
	s_addc_u32 s27, s67, 0
	s_add_i32 s16, s17, s9
	global_load_lds_dwordx4 v[158:159], off
	v_lshl_add_u64 v[158:159], s[26:27], 0, v[150:151]
	s_mov_b32 m0, s16
	s_nop 0
	global_load_lds_dwordx4 v[158:159], off
	v_lshl_add_u64 v[158:159], s[26:27], 0, v[154:155]
	s_add_i32 m0, s16, 0x2000
	s_nop 0
	global_load_lds_dwordx4 v[158:159], off
	v_lshl_add_u64 v[158:159], s[64:65], 0, v[148:149]
	s_mov_b32 m0, s86
	s_nop 0
	global_load_lds_dwordx4 v[158:159], off
	v_lshl_add_u64 v[158:159], s[64:65], 0, v[152:153]
	s_mov_b32 m0, s87
	s_nop 0
	global_load_lds_dwordx4 v[158:159], off
	s_waitcnt vmcnt(8)
	s_waitcnt lgkmcnt(0)
	s_barrier
	s_setprio 3
	s_waitcnt lgkmcnt(0)
	v_mfma_f32_16x16x32_bf16 v[62:65], v[82:85], v[222:225], v[62:65]
	v_mfma_f32_16x16x32_bf16 v[58:61], v[90:93], v[222:225], v[58:61]
	v_mfma_f32_16x16x32_bf16 v[46:49], v[82:85], v[230:233], v[46:49]
	v_mfma_f32_16x16x32_bf16 v[42:45], v[90:93], v[230:233], v[42:45]
	v_mfma_f32_16x16x32_bf16 v[30:33], v[82:85], v[238:241], v[30:33]
	v_mfma_f32_16x16x32_bf16 v[26:29], v[90:93], v[238:241], v[26:29]
	v_mfma_f32_16x16x32_bf16 v[14:17], v[82:85], v[246:249], v[14:17]
	v_mfma_f32_16x16x32_bf16 v[10:13], v[90:93], v[246:249], v[10:13]
	v_mfma_f32_16x16x32_bf16 v[62:65], v[86:89], v[226:229], v[62:65]
	v_mfma_f32_16x16x32_bf16 v[58:61], v[94:97], v[226:229], v[58:61]
	v_mfma_f32_16x16x32_bf16 v[46:49], v[86:89], v[234:237], v[46:49]
	v_mfma_f32_16x16x32_bf16 v[42:45], v[94:97], v[234:237], v[42:45]
	v_mfma_f32_16x16x32_bf16 v[30:33], v[86:89], v[242:245], v[30:33]
	v_mfma_f32_16x16x32_bf16 v[26:29], v[94:97], v[242:245], v[26:29]
	v_mfma_f32_16x16x32_bf16 v[14:17], v[86:89], v[250:253], v[14:17]
	v_mfma_f32_16x16x32_bf16 v[10:13], v[94:97], v[250:253], v[10:13]
	s_setprio 0
	s_setprio 3
	v_mfma_f32_16x16x32_bf16 v[54:57], v[174:177], v[222:225], v[54:57]
	v_mfma_f32_16x16x32_bf16 v[50:53], v[214:217], v[222:225], v[50:53]
	v_mfma_f32_16x16x32_bf16 v[38:41], v[174:177], v[230:233], v[38:41]
	v_mfma_f32_16x16x32_bf16 v[34:37], v[214:217], v[230:233], v[34:37]
	v_mfma_f32_16x16x32_bf16 v[22:25], v[174:177], v[238:241], v[22:25]
	v_mfma_f32_16x16x32_bf16 v[18:21], v[214:217], v[238:241], v[18:21]
	v_mfma_f32_16x16x32_bf16 v[6:9], v[174:177], v[246:249], v[6:9]
	v_mfma_f32_16x16x32_bf16 v[2:5], v[214:217], v[246:249], v[2:5]
	v_mfma_f32_16x16x32_bf16 v[54:57], v[178:181], v[226:229], v[54:57]
	v_mfma_f32_16x16x32_bf16 v[50:53], v[218:221], v[226:229], v[50:53]
	v_mfma_f32_16x16x32_bf16 v[38:41], v[178:181], v[234:237], v[38:41]
	v_mfma_f32_16x16x32_bf16 v[34:37], v[218:221], v[234:237], v[34:37]
	v_mfma_f32_16x16x32_bf16 v[22:25], v[178:181], v[242:245], v[22:25]
	v_mfma_f32_16x16x32_bf16 v[18:21], v[218:221], v[242:245], v[18:21]
	v_mfma_f32_16x16x32_bf16 v[6:9], v[178:181], v[250:253], v[6:9]
	v_mfma_f32_16x16x32_bf16 v[2:5], v[218:221], v[250:253], v[2:5]
	s_setprio 0
	s_barrier
	s_add_i32 vcc_hi, vcc_hi, 2
	s_add_u32 s62, s62, 0x10000
	s_addc_u32 s63, s63, 0
	s_add_u32 s61, s61, 0x10000
	s_addc_u32 vcc_lo, vcc_lo, 0
	s_cmp_gt_u32 vcc_hi, 29
	s_cbranch_scc0 .LBB0_171
	s_and_b64 vcc, exec, s[48:49]
	s_cbranch_vccz .LBB0_174
	s_barrier

.Lrx_hgrn1_w0:
	s_waitcnt vmcnt(24)
	s_waitcnt lgkmcnt(0)
	s_barrier
	s_setprio 3
	s_waitcnt lgkmcnt(0)
	v_mfma_f32_16x16x32_bf16 v[128:131], v[132:135], v[202:205], v[128:131]
	v_mfma_f32_16x16x32_bf16 v[124:127], v[152:155], v[202:205], v[124:127]
	v_mfma_f32_16x16x32_bf16 v[110:113], v[132:135], v[210:213], v[110:113]
	v_mfma_f32_16x16x32_bf16 v[106:109], v[152:155], v[210:213], v[106:109]
	v_mfma_f32_16x16x32_bf16 v[94:97], v[132:135], v[218:221], v[94:97]
	v_mfma_f32_16x16x32_bf16 v[90:93], v[152:155], v[218:221], v[90:93]
	v_mfma_f32_16x16x32_bf16 v[78:81], v[132:135], v[226:229], v[78:81]
	v_mfma_f32_16x16x32_bf16 v[74:77], v[152:155], v[226:229], v[74:77]
	v_mfma_f32_16x16x32_bf16 v[128:131], v[136:139], v[206:209], v[128:131]
	v_mfma_f32_16x16x32_bf16 v[124:127], v[166:169], v[206:209], v[124:127]
	v_mfma_f32_16x16x32_bf16 v[110:113], v[136:139], v[214:217], v[110:113]
	v_mfma_f32_16x16x32_bf16 v[106:109], v[166:169], v[214:217], v[106:109]
	v_mfma_f32_16x16x32_bf16 v[94:97], v[136:139], v[222:225], v[94:97]
	v_mfma_f32_16x16x32_bf16 v[90:93], v[166:169], v[222:225], v[90:93]
	v_mfma_f32_16x16x32_bf16 v[78:81], v[136:139], v[230:233], v[78:81]
	v_mfma_f32_16x16x32_bf16 v[74:77], v[166:169], v[230:233], v[74:77]
	s_setprio 0
	s_setprio 3
	v_mfma_f32_16x16x32_bf16 v[120:123], v[176:179], v[202:205], v[120:123]
	v_mfma_f32_16x16x32_bf16 v[116:119], v[194:197], v[202:205], v[116:119]
	v_mfma_f32_16x16x32_bf16 v[102:105], v[176:179], v[210:213], v[102:105]
	v_mfma_f32_16x16x32_bf16 v[98:101], v[194:197], v[210:213], v[98:101]
	v_mfma_f32_16x16x32_bf16 v[86:89], v[176:179], v[218:221], v[86:89]
	v_mfma_f32_16x16x32_bf16 v[82:85], v[194:197], v[218:221], v[82:85]
	v_mfma_f32_16x16x32_bf16 v[70:73], v[176:179], v[226:229], v[70:73]
	v_mfma_f32_16x16x32_bf16 v[66:69], v[194:197], v[226:229], v[66:69]
	v_mfma_f32_16x16x32_bf16 v[120:123], v[180:183], v[206:209], v[120:123]
	v_mfma_f32_16x16x32_bf16 v[116:119], v[198:201], v[206:209], v[116:119]
	v_mfma_f32_16x16x32_bf16 v[102:105], v[180:183], v[214:217], v[102:105]
	v_mfma_f32_16x16x32_bf16 v[98:101], v[198:201], v[214:217], v[98:101]
	v_mfma_f32_16x16x32_bf16 v[86:89], v[180:183], v[222:225], v[86:89]
	v_mfma_f32_16x16x32_bf16 v[82:85], v[198:201], v[222:225], v[82:85]
	v_mfma_f32_16x16x32_bf16 v[70:73], v[180:183], v[230:233], v[70:73]
	v_mfma_f32_16x16x32_bf16 v[66:69], v[198:201], v[230:233], v[66:69]
	s_setprio 0
	s_barrier
	s_add_i32 s16, s16, s4
	v_lshl_add_u64 v[158:159], s[60:61], 0, v[142:143]
	s_mov_b32 m0, s16
	ds_read_b128 v[202:205], v175 offset:16384
	ds_read_b128 v[206:209], v175 offset:17408
	ds_read_b128 v[210:213], v175 offset:18432
	ds_read_b128 v[214:217], v175 offset:19456
	ds_read_b128 v[218:221], v175 offset:20480
	ds_read_b128 v[222:225], v175 offset:21504
	ds_read_b128 v[226:229], v175 offset:22528
	ds_read_b128 v[230:233], v175 offset:23552
	global_load_lds_dwordx4 v[158:159], off
	s_add_i32 m0, s16, 0x2000
	s_add_u32 s74, s60, 0x1000
	v_lshl_add_u64 v[158:159], s[60:61], 0, v[146:147]
	s_addc_u32 s75, s61, 0
	s_add_i32 s16, s17, s4
	global_load_lds_dwordx4 v[158:159], off
	v_lshl_add_u64 v[158:159], s[74:75], 0, v[142:143]
	s_mov_b32 m0, s16
	s_nop 0
	global_load_lds_dwordx4 v[158:159], off
	v_lshl_add_u64 v[158:159], s[74:75], 0, v[146:147]
	s_add_i32 m0, s16, 0x2000
	s_nop 0
	global_load_lds_dwordx4 v[158:159], off
	v_lshl_add_u64 v[158:159], s[62:63], 0, v[140:141]
	s_mov_b32 m0, s13
	s_nop 0
	global_load_lds_dwordx4 v[158:159], off
	v_lshl_add_u64 v[158:159], s[62:63], 0, v[144:145]
	s_mov_b32 m0, s20
	s_nop 0
	global_load_lds_dwordx4 v[158:159], off
	s_cmp_lg_u32 s32, 0
	s_cbranch_scc1 .Lrx_hgrn1_w1
	s_waitcnt vmcnt(8)
.Lrx_hgrn1_w1:
	s_waitcnt vmcnt(24)
	s_waitcnt lgkmcnt(0)
	s_barrier
	s_setprio 3
	s_waitcnt lgkmcnt(0)
	v_mfma_f32_16x16x32_bf16 v[62:65], v[132:135], v[202:205], v[62:65]
	v_mfma_f32_16x16x32_bf16 v[58:61], v[152:155], v[202:205], v[58:61]
	v_mfma_f32_16x16x32_bf16 v[46:49], v[132:135], v[210:213], v[46:49]
	v_mfma_f32_16x16x32_bf16 v[42:45], v[152:155], v[210:213], v[42:45]
	v_mfma_f32_16x16x32_bf16 v[30:33], v[132:135], v[218:221], v[30:33]
	v_mfma_f32_16x16x32_bf16 v[26:29], v[152:155], v[218:221], v[26:29]
	v_mfma_f32_16x16x32_bf16 v[14:17], v[132:135], v[226:229], v[14:17]
	v_mfma_f32_16x16x32_bf16 v[10:13], v[152:155], v[226:229], v[10:13]
	v_mfma_f32_16x16x32_bf16 v[62:65], v[136:139], v[206:209], v[62:65]
	v_mfma_f32_16x16x32_bf16 v[58:61], v[166:169], v[206:209], v[58:61]
	v_mfma_f32_16x16x32_bf16 v[46:49], v[136:139], v[214:217], v[46:49]
	v_mfma_f32_16x16x32_bf16 v[42:45], v[166:169], v[214:217], v[42:45]
	v_mfma_f32_16x16x32_bf16 v[30:33], v[136:139], v[222:225], v[30:33]
	v_mfma_f32_16x16x32_bf16 v[26:29], v[166:169], v[222:225], v[26:29]
	v_mfma_f32_16x16x32_bf16 v[14:17], v[136:139], v[230:233], v[14:17]
	v_mfma_f32_16x16x32_bf16 v[10:13], v[166:169], v[230:233], v[10:13]
	s_setprio 0
	s_setprio 3
	v_mfma_f32_16x16x32_bf16 v[54:57], v[176:179], v[202:205], v[54:57]
	v_mfma_f32_16x16x32_bf16 v[50:53], v[194:197], v[202:205], v[50:53]
	v_mfma_f32_16x16x32_bf16 v[38:41], v[176:179], v[210:213], v[38:41]
	v_mfma_f32_16x16x32_bf16 v[34:37], v[194:197], v[210:213], v[34:37]
	v_mfma_f32_16x16x32_bf16 v[22:25], v[176:179], v[218:221], v[22:25]
	v_mfma_f32_16x16x32_bf16 v[18:21], v[194:197], v[218:221], v[18:21]
	v_mfma_f32_16x16x32_bf16 v[6:9], v[176:179], v[226:229], v[6:9]
	v_mfma_f32_16x16x32_bf16 v[2:5], v[194:197], v[226:229], v[2:5]
	v_mfma_f32_16x16x32_bf16 v[54:57], v[180:183], v[206:209], v[54:57]
	v_mfma_f32_16x16x32_bf16 v[50:53], v[198:201], v[206:209], v[50:53]
	v_mfma_f32_16x16x32_bf16 v[38:41], v[180:183], v[214:217], v[38:41]
	v_mfma_f32_16x16x32_bf16 v[34:37], v[198:201], v[214:217], v[34:37]
	v_mfma_f32_16x16x32_bf16 v[22:25], v[180:183], v[222:225], v[22:25]
	v_mfma_f32_16x16x32_bf16 v[18:21], v[198:201], v[222:225], v[18:21]
	v_mfma_f32_16x16x32_bf16 v[6:9], v[180:183], v[230:233], v[6:9]
	v_mfma_f32_16x16x32_bf16 v[2:5], v[198:201], v[230:233], v[2:5]
	s_setprio 0
	s_barrier
	s_add_i32 s16, 0, 0x18000
	v_add_u32_e32 v114, s16, v172
	s_add_i32 s17, 0, 0x1c000
	ds_read_b128 v[132:135], v114
	ds_read_b128 v[136:139], v114 offset:1024
	ds_read_b128 v[152:155], v114 offset:2048
	ds_read_b128 v[166:169], v114 offset:3072
	v_add_u32_e32 v114, s17, v172
	ds_read_b128 v[176:179], v114
	ds_read_b128 v[180:183], v114 offset:1024
	ds_read_b128 v[194:197], v114 offset:2048
	ds_read_b128 v[198:201], v114 offset:3072
	s_add_u32 s62, s62, 0x4000
	s_addc_u32 s63, s63, 0
	s_mov_b32 m0, s21
	v_lshl_add_u64 v[158:159], s[62:63], 0, v[140:141]
	ds_read_b128 v[202:205], v175 offset:32768
	ds_read_b128 v[206:209], v175 offset:33792
	ds_read_b128 v[210:213], v175 offset:34816
	ds_read_b128 v[214:217], v175 offset:35840
	ds_read_b128 v[218:221], v175 offset:36864
	ds_read_b128 v[222:225], v175 offset:37888
	ds_read_b128 v[226:229], v175 offset:38912
	ds_read_b128 v[230:233], v175 offset:39936
	global_load_lds_dwordx4 v[158:159], off
	v_lshl_add_u64 v[158:159], s[62:63], 0, v[144:145]
	s_mov_b32 m0, s24
	s_nop 0
	global_load_lds_dwordx4 v[158:159], off
	s_cmp_lg_u32 s32, 0
	s_cbranch_scc1 .Lrx_hgrn1_w2
	s_waitcnt vmcnt(8)
.Lrx_hgrn1_w2:
	s_waitcnt vmcnt(24)
	s_mov_b32 s32, 0
	s_waitcnt lgkmcnt(0)
	s_barrier
	s_setprio 3
	s_waitcnt lgkmcnt(0)
	v_mfma_f32_16x16x32_bf16 v[128:131], v[132:135], v[202:205], v[128:131]
	v_mfma_f32_16x16x32_bf16 v[124:127], v[152:155], v[202:205], v[124:127]
	v_mfma_f32_16x16x32_bf16 v[110:113], v[132:135], v[210:213], v[110:113]
	v_mfma_f32_16x16x32_bf16 v[106:109], v[152:155], v[210:213], v[106:109]
	v_mfma_f32_16x16x32_bf16 v[94:97], v[132:135], v[218:221], v[94:97]
	v_mfma_f32_16x16x32_bf16 v[90:93], v[152:155], v[218:221], v[90:93]
	v_mfma_f32_16x16x32_bf16 v[78:81], v[132:135], v[226:229], v[78:81]
	v_mfma_f32_16x16x32_bf16 v[74:77], v[152:155], v[226:229], v[74:77]
	v_mfma_f32_16x16x32_bf16 v[128:131], v[136:139], v[206:209], v[128:131]
	v_mfma_f32_16x16x32_bf16 v[124:127], v[166:169], v[206:209], v[124:127]
	v_mfma_f32_16x16x32_bf16 v[110:113], v[136:139], v[214:217], v[110:113]
	v_mfma_f32_16x16x32_bf16 v[106:109], v[166:169], v[214:217], v[106:109]
	v_mfma_f32_16x16x32_bf16 v[94:97], v[136:139], v[222:225], v[94:97]
	v_mfma_f32_16x16x32_bf16 v[90:93], v[166:169], v[222:225], v[90:93]
	v_mfma_f32_16x16x32_bf16 v[78:81], v[136:139], v[230:233], v[78:81]
	v_mfma_f32_16x16x32_bf16 v[74:77], v[166:169], v[230:233], v[74:77]
	s_setprio 0
	s_setprio 3
	v_mfma_f32_16x16x32_bf16 v[120:123], v[176:179], v[202:205], v[120:123]
	v_mfma_f32_16x16x32_bf16 v[116:119], v[194:197], v[202:205], v[116:119]
	v_mfma_f32_16x16x32_bf16 v[102:105], v[176:179], v[210:213], v[102:105]
	v_mfma_f32_16x16x32_bf16 v[98:101], v[194:197], v[210:213], v[98:101]
	v_mfma_f32_16x16x32_bf16 v[86:89], v[176:179], v[218:221], v[86:89]
	v_mfma_f32_16x16x32_bf16 v[82:85], v[194:197], v[218:221], v[82:85]
	v_mfma_f32_16x16x32_bf16 v[70:73], v[176:179], v[226:229], v[70:73]
	v_mfma_f32_16x16x32_bf16 v[66:69], v[194:197], v[226:229], v[66:69]
	v_mfma_f32_16x16x32_bf16 v[120:123], v[180:183], v[206:209], v[120:123]
	v_mfma_f32_16x16x32_bf16 v[116:119], v[198:201], v[206:209], v[116:119]
	v_mfma_f32_16x16x32_bf16 v[102:105], v[180:183], v[214:217], v[102:105]
	v_mfma_f32_16x16x32_bf16 v[98:101], v[198:201], v[214:217], v[98:101]
	v_mfma_f32_16x16x32_bf16 v[86:89], v[180:183], v[222:225], v[86:89]
	v_mfma_f32_16x16x32_bf16 v[82:85], v[198:201], v[222:225], v[82:85]
	v_mfma_f32_16x16x32_bf16 v[70:73], v[180:183], v[230:233], v[70:73]
	v_mfma_f32_16x16x32_bf16 v[66:69], v[198:201], v[230:233], v[66:69]
	s_setprio 0
	s_barrier
	s_add_u32 s62, s60, 0x8000
	s_addc_u32 s63, s61, 0
	s_add_i32 s16, s16, s4
	v_lshl_add_u64 v[158:159], s[62:63], 0, v[142:143]
	s_mov_b32 m0, s16
	ds_read_b128 v[202:205], v175 offset:49152
	ds_read_b128 v[206:209], v175 offset:50176
	ds_read_b128 v[210:213], v175 offset:51200
	ds_read_b128 v[214:217], v175 offset:52224
	ds_read_b128 v[218:221], v175 offset:53248
	ds_read_b128 v[222:225], v175 offset:54272
	ds_read_b128 v[226:229], v175 offset:55296
	ds_read_b128 v[230:233], v175 offset:56320
	global_load_lds_dwordx4 v[158:159], off
	s_add_i32 m0, s16, 0x2000
	s_add_u32 s60, s60, 0x9000
	v_lshl_add_u64 v[158:159], s[62:63], 0, v[146:147]
	s_addc_u32 s61, s61, 0
	s_add_i32 s16, s17, s4
	global_load_lds_dwordx4 v[158:159], off
	v_lshl_add_u64 v[158:159], s[60:61], 0, v[142:143]
	s_mov_b32 m0, s16
	s_nop 0
	global_load_lds_dwordx4 v[158:159], off
	v_lshl_add_u64 v[158:159], s[60:61], 0, v[146:147]
	s_add_i32 m0, s16, 0x2000
	s_nop 0
	global_load_lds_dwordx4 v[158:159], off
	v_lshl_add_u64 v[158:159], s[58:59], 0, v[140:141]
	s_mov_b32 m0, s65
	s_nop 0
	global_load_lds_dwordx4 v[158:159], off
	v_lshl_add_u64 v[158:159], s[58:59], 0, v[144:145]
	s_mov_b32 m0, s66
	s_nop 0
	global_load_lds_dwordx4 v[158:159], off
	s_waitcnt vmcnt(8)
	s_waitcnt lgkmcnt(0)
	s_barrier
	s_setprio 3
	s_waitcnt lgkmcnt(0)
	v_mfma_f32_16x16x32_bf16 v[62:65], v[132:135], v[202:205], v[62:65]
	v_mfma_f32_16x16x32_bf16 v[58:61], v[152:155], v[202:205], v[58:61]
	v_mfma_f32_16x16x32_bf16 v[46:49], v[132:135], v[210:213], v[46:49]
	v_mfma_f32_16x16x32_bf16 v[42:45], v[152:155], v[210:213], v[42:45]
	v_mfma_f32_16x16x32_bf16 v[30:33], v[132:135], v[218:221], v[30:33]
	v_mfma_f32_16x16x32_bf16 v[26:29], v[152:155], v[218:221], v[26:29]
	v_mfma_f32_16x16x32_bf16 v[14:17], v[132:135], v[226:229], v[14:17]
	v_mfma_f32_16x16x32_bf16 v[10:13], v[152:155], v[226:229], v[10:13]
	v_mfma_f32_16x16x32_bf16 v[62:65], v[136:139], v[206:209], v[62:65]
	v_mfma_f32_16x16x32_bf16 v[58:61], v[166:169], v[206:209], v[58:61]
	v_mfma_f32_16x16x32_bf16 v[46:49], v[136:139], v[214:217], v[46:49]
	v_mfma_f32_16x16x32_bf16 v[42:45], v[166:169], v[214:217], v[42:45]
	v_mfma_f32_16x16x32_bf16 v[30:33], v[136:139], v[222:225], v[30:33]
	v_mfma_f32_16x16x32_bf16 v[26:29], v[166:169], v[222:225], v[26:29]
	v_mfma_f32_16x16x32_bf16 v[14:17], v[136:139], v[230:233], v[14:17]
	v_mfma_f32_16x16x32_bf16 v[10:13], v[166:169], v[230:233], v[10:13]
	s_setprio 0
	s_setprio 3
	v_mfma_f32_16x16x32_bf16 v[54:57], v[176:179], v[202:205], v[54:57]
	v_mfma_f32_16x16x32_bf16 v[50:53], v[194:197], v[202:205], v[50:53]
	v_mfma_f32_16x16x32_bf16 v[38:41], v[176:179], v[210:213], v[38:41]
	v_mfma_f32_16x16x32_bf16 v[34:37], v[194:197], v[210:213], v[34:37]
	v_mfma_f32_16x16x32_bf16 v[22:25], v[176:179], v[218:221], v[22:25]
	v_mfma_f32_16x16x32_bf16 v[18:21], v[194:197], v[218:221], v[18:21]
	v_mfma_f32_16x16x32_bf16 v[6:9], v[176:179], v[226:229], v[6:9]
	v_mfma_f32_16x16x32_bf16 v[2:5], v[194:197], v[226:229], v[2:5]
	v_mfma_f32_16x16x32_bf16 v[54:57], v[180:183], v[206:209], v[54:57]
	v_mfma_f32_16x16x32_bf16 v[50:53], v[198:201], v[206:209], v[50:53]
	v_mfma_f32_16x16x32_bf16 v[38:41], v[180:183], v[214:217], v[38:41]
	v_mfma_f32_16x16x32_bf16 v[34:37], v[198:201], v[214:217], v[34:37]
	v_mfma_f32_16x16x32_bf16 v[22:25], v[180:183], v[222:225], v[22:25]
	v_mfma_f32_16x16x32_bf16 v[18:21], v[198:201], v[222:225], v[18:21]
	v_mfma_f32_16x16x32_bf16 v[6:9], v[180:183], v[230:233], v[6:9]
	v_mfma_f32_16x16x32_bf16 v[2:5], v[198:201], v[230:233], v[2:5]
	s_setprio 0
	s_barrier
	s_add_i32 s70, s70, 2
	s_add_u32 s56, s56, 0x10000
	s_addc_u32 s57, s57, 0
	s_add_u32 s51, s51, 0x10000
	s_addc_u32 s69, s69, 0
	s_cmp_gt_u32 s70, 29
	s_cbranch_scc0 .LBB0_346
	s_add_u32 s100, s29, 0xc000
	s_addc_u32 s101, s15, 0
	v_lshl_add_u64 v[158:159], s[100:101], 0, v[148:149]
	s_add_i32 m0, s13, 0xc000
	s_nop 0
	global_load_lds_dwordx4 v[158:159], off
	v_lshl_add_u64 v[158:159], s[100:101], 0, v[150:151]
	s_add_i32 m0, s13, 0xe000
	s_nop 0
	global_load_lds_dwordx4 v[158:159], off
	s_and_b64 vcc, exec, s[46:47]
	s_cbranch_vccz .LBB0_349
	s_barrier

.Lrx_hgrn2_w0:
	s_waitcnt vmcnt(24)
	s_waitcnt lgkmcnt(0)
	s_barrier
	s_setprio 3
	s_waitcnt lgkmcnt(0)
	v_mfma_f32_16x16x32_bf16 v[128:131], v[132:135], v[202:205], v[128:131]
	v_mfma_f32_16x16x32_bf16 v[124:127], v[152:155], v[202:205], v[124:127]
	v_mfma_f32_16x16x32_bf16 v[110:113], v[132:135], v[210:213], v[110:113]
	v_mfma_f32_16x16x32_bf16 v[106:109], v[152:155], v[210:213], v[106:109]
	v_mfma_f32_16x16x32_bf16 v[94:97], v[132:135], v[218:221], v[94:97]
	v_mfma_f32_16x16x32_bf16 v[90:93], v[152:155], v[218:221], v[90:93]
	v_mfma_f32_16x16x32_bf16 v[78:81], v[132:135], v[226:229], v[78:81]
	v_mfma_f32_16x16x32_bf16 v[74:77], v[152:155], v[226:229], v[74:77]
	v_mfma_f32_16x16x32_bf16 v[128:131], v[136:139], v[206:209], v[128:131]
	v_mfma_f32_16x16x32_bf16 v[124:127], v[166:169], v[206:209], v[124:127]
	v_mfma_f32_16x16x32_bf16 v[110:113], v[136:139], v[214:217], v[110:113]
	v_mfma_f32_16x16x32_bf16 v[106:109], v[166:169], v[214:217], v[106:109]
	v_mfma_f32_16x16x32_bf16 v[94:97], v[136:139], v[222:225], v[94:97]
	v_mfma_f32_16x16x32_bf16 v[90:93], v[166:169], v[222:225], v[90:93]
	v_mfma_f32_16x16x32_bf16 v[78:81], v[136:139], v[230:233], v[78:81]
	v_mfma_f32_16x16x32_bf16 v[74:77], v[166:169], v[230:233], v[74:77]
	s_setprio 0
	s_setprio 3
	v_mfma_f32_16x16x32_bf16 v[120:123], v[176:179], v[202:205], v[120:123]
	v_mfma_f32_16x16x32_bf16 v[116:119], v[194:197], v[202:205], v[116:119]
	v_mfma_f32_16x16x32_bf16 v[102:105], v[176:179], v[210:213], v[102:105]
	v_mfma_f32_16x16x32_bf16 v[98:101], v[194:197], v[210:213], v[98:101]
	v_mfma_f32_16x16x32_bf16 v[86:89], v[176:179], v[218:221], v[86:89]
	v_mfma_f32_16x16x32_bf16 v[82:85], v[194:197], v[218:221], v[82:85]
	v_mfma_f32_16x16x32_bf16 v[70:73], v[176:179], v[226:229], v[70:73]
	v_mfma_f32_16x16x32_bf16 v[66:69], v[194:197], v[226:229], v[66:69]
	v_mfma_f32_16x16x32_bf16 v[120:123], v[180:183], v[206:209], v[120:123]
	v_mfma_f32_16x16x32_bf16 v[116:119], v[198:201], v[206:209], v[116:119]
	v_mfma_f32_16x16x32_bf16 v[102:105], v[180:183], v[214:217], v[102:105]
	v_mfma_f32_16x16x32_bf16 v[98:101], v[198:201], v[214:217], v[98:101]
	v_mfma_f32_16x16x32_bf16 v[86:89], v[180:183], v[222:225], v[86:89]
	v_mfma_f32_16x16x32_bf16 v[82:85], v[198:201], v[222:225], v[82:85]
	v_mfma_f32_16x16x32_bf16 v[70:73], v[180:183], v[230:233], v[70:73]
	v_mfma_f32_16x16x32_bf16 v[66:69], v[198:201], v[230:233], v[66:69]
	s_setprio 0
	s_barrier
	s_add_i32 s16, s16, s4
	v_lshl_add_u64 v[158:159], s[58:59], 0, v[142:143]
	s_mov_b32 m0, s16
	ds_read_b128 v[202:205], v175 offset:16384
	ds_read_b128 v[206:209], v175 offset:17408
	ds_read_b128 v[210:213], v175 offset:18432
	ds_read_b128 v[214:217], v175 offset:19456
	ds_read_b128 v[218:221], v175 offset:20480
	ds_read_b128 v[222:225], v175 offset:21504
	ds_read_b128 v[226:229], v175 offset:22528
	ds_read_b128 v[230:233], v175 offset:23552
	global_load_lds_dwordx4 v[158:159], off
	s_add_i32 m0, s16, 0x2000
	s_add_u32 s68, s58, 0x1000
	v_lshl_add_u64 v[158:159], s[58:59], 0, v[146:147]
	s_addc_u32 s69, s59, 0
	s_add_i32 s16, s17, s4
	global_load_lds_dwordx4 v[158:159], off
	v_lshl_add_u64 v[158:159], s[68:69], 0, v[142:143]
	s_mov_b32 m0, s16
	s_nop 0
	global_load_lds_dwordx4 v[158:159], off
	v_lshl_add_u64 v[158:159], s[68:69], 0, v[146:147]
	s_add_i32 m0, s16, 0x2000
	s_nop 0
	global_load_lds_dwordx4 v[158:159], off
	v_lshl_add_u64 v[158:159], s[60:61], 0, v[140:141]
	s_mov_b32 m0, s12
	s_nop 0
	global_load_lds_dwordx4 v[158:159], off
	v_lshl_add_u64 v[158:159], s[60:61], 0, v[144:145]
	s_mov_b32 m0, s13
	s_nop 0
	global_load_lds_dwordx4 v[158:159], off
	s_cmp_lg_u32 s32, 0
	s_cbranch_scc1 .Lrx_hgrn2_w1
	s_waitcnt vmcnt(8)
.Lrx_hgrn2_w1:
	s_waitcnt vmcnt(24)
	s_waitcnt lgkmcnt(0)
	s_barrier
	s_setprio 3
	s_waitcnt lgkmcnt(0)
	v_mfma_f32_16x16x32_bf16 v[62:65], v[132:135], v[202:205], v[62:65]
	v_mfma_f32_16x16x32_bf16 v[58:61], v[152:155], v[202:205], v[58:61]
	v_mfma_f32_16x16x32_bf16 v[46:49], v[132:135], v[210:213], v[46:49]
	v_mfma_f32_16x16x32_bf16 v[42:45], v[152:155], v[210:213], v[42:45]
	v_mfma_f32_16x16x32_bf16 v[30:33], v[132:135], v[218:221], v[30:33]
	v_mfma_f32_16x16x32_bf16 v[26:29], v[152:155], v[218:221], v[26:29]
	v_mfma_f32_16x16x32_bf16 v[14:17], v[132:135], v[226:229], v[14:17]
	v_mfma_f32_16x16x32_bf16 v[10:13], v[152:155], v[226:229], v[10:13]
	v_mfma_f32_16x16x32_bf16 v[62:65], v[136:139], v[206:209], v[62:65]
	v_mfma_f32_16x16x32_bf16 v[58:61], v[166:169], v[206:209], v[58:61]
	v_mfma_f32_16x16x32_bf16 v[46:49], v[136:139], v[214:217], v[46:49]
	v_mfma_f32_16x16x32_bf16 v[42:45], v[166:169], v[214:217], v[42:45]
	v_mfma_f32_16x16x32_bf16 v[30:33], v[136:139], v[222:225], v[30:33]
	v_mfma_f32_16x16x32_bf16 v[26:29], v[166:169], v[222:225], v[26:29]
	v_mfma_f32_16x16x32_bf16 v[14:17], v[136:139], v[230:233], v[14:17]
	v_mfma_f32_16x16x32_bf16 v[10:13], v[166:169], v[230:233], v[10:13]
	s_setprio 0
	s_setprio 3
	v_mfma_f32_16x16x32_bf16 v[54:57], v[176:179], v[202:205], v[54:57]
	v_mfma_f32_16x16x32_bf16 v[50:53], v[194:197], v[202:205], v[50:53]
	v_mfma_f32_16x16x32_bf16 v[38:41], v[176:179], v[210:213], v[38:41]
	v_mfma_f32_16x16x32_bf16 v[34:37], v[194:197], v[210:213], v[34:37]
	v_mfma_f32_16x16x32_bf16 v[22:25], v[176:179], v[218:221], v[22:25]
	v_mfma_f32_16x16x32_bf16 v[18:21], v[194:197], v[218:221], v[18:21]
	v_mfma_f32_16x16x32_bf16 v[6:9], v[176:179], v[226:229], v[6:9]
	v_mfma_f32_16x16x32_bf16 v[2:5], v[194:197], v[226:229], v[2:5]
	v_mfma_f32_16x16x32_bf16 v[54:57], v[180:183], v[206:209], v[54:57]
	v_mfma_f32_16x16x32_bf16 v[50:53], v[198:201], v[206:209], v[50:53]
	v_mfma_f32_16x16x32_bf16 v[38:41], v[180:183], v[214:217], v[38:41]
	v_mfma_f32_16x16x32_bf16 v[34:37], v[198:201], v[214:217], v[34:37]
	v_mfma_f32_16x16x32_bf16 v[22:25], v[180:183], v[222:225], v[22:25]
	v_mfma_f32_16x16x32_bf16 v[18:21], v[198:201], v[222:225], v[18:21]
	v_mfma_f32_16x16x32_bf16 v[6:9], v[180:183], v[230:233], v[6:9]
	v_mfma_f32_16x16x32_bf16 v[2:5], v[198:201], v[230:233], v[2:5]
	s_setprio 0
	s_barrier
	s_add_i32 s16, 0, 0x18000
	v_add_u32_e32 v114, s16, v172
	s_add_i32 s17, 0, 0x1c000
	ds_read_b128 v[132:135], v114
	ds_read_b128 v[136:139], v114 offset:1024
	ds_read_b128 v[152:155], v114 offset:2048
	ds_read_b128 v[166:169], v114 offset:3072
	v_add_u32_e32 v114, s17, v172
	ds_read_b128 v[176:179], v114
	ds_read_b128 v[180:183], v114 offset:1024
	ds_read_b128 v[194:197], v114 offset:2048
	ds_read_b128 v[198:201], v114 offset:3072
	s_add_u32 s60, s60, 0x4000
	s_addc_u32 s61, s61, 0
	s_mov_b32 m0, s20
	v_lshl_add_u64 v[158:159], s[60:61], 0, v[140:141]
	ds_read_b128 v[202:205], v175 offset:32768
	ds_read_b128 v[206:209], v175 offset:33792
	ds_read_b128 v[210:213], v175 offset:34816
	ds_read_b128 v[214:217], v175 offset:35840
	ds_read_b128 v[218:221], v175 offset:36864
	ds_read_b128 v[222:225], v175 offset:37888
	ds_read_b128 v[226:229], v175 offset:38912
	ds_read_b128 v[230:233], v175 offset:39936
	global_load_lds_dwordx4 v[158:159], off
	v_lshl_add_u64 v[158:159], s[60:61], 0, v[144:145]
	s_mov_b32 m0, s21
	s_nop 0
	global_load_lds_dwordx4 v[158:159], off
	s_cmp_lg_u32 s32, 0
	s_cbranch_scc1 .Lrx_hgrn2_w2
	s_waitcnt vmcnt(8)
.Lrx_hgrn2_w2:
	s_waitcnt vmcnt(24)
	s_mov_b32 s32, 0
	s_waitcnt lgkmcnt(0)
	s_barrier
	s_setprio 3
	s_waitcnt lgkmcnt(0)
	v_mfma_f32_16x16x32_bf16 v[128:131], v[132:135], v[202:205], v[128:131]
	v_mfma_f32_16x16x32_bf16 v[124:127], v[152:155], v[202:205], v[124:127]
	v_mfma_f32_16x16x32_bf16 v[110:113], v[132:135], v[210:213], v[110:113]
	v_mfma_f32_16x16x32_bf16 v[106:109], v[152:155], v[210:213], v[106:109]
	v_mfma_f32_16x16x32_bf16 v[94:97], v[132:135], v[218:221], v[94:97]
	v_mfma_f32_16x16x32_bf16 v[90:93], v[152:155], v[218:221], v[90:93]
	v_mfma_f32_16x16x32_bf16 v[78:81], v[132:135], v[226:229], v[78:81]
	v_mfma_f32_16x16x32_bf16 v[74:77], v[152:155], v[226:229], v[74:77]
	v_mfma_f32_16x16x32_bf16 v[128:131], v[136:139], v[206:209], v[128:131]
	v_mfma_f32_16x16x32_bf16 v[124:127], v[166:169], v[206:209], v[124:127]
	v_mfma_f32_16x16x32_bf16 v[110:113], v[136:139], v[214:217], v[110:113]
	v_mfma_f32_16x16x32_bf16 v[106:109], v[166:169], v[214:217], v[106:109]
	v_mfma_f32_16x16x32_bf16 v[94:97], v[136:139], v[222:225], v[94:97]
	v_mfma_f32_16x16x32_bf16 v[90:93], v[166:169], v[222:225], v[90:93]
	v_mfma_f32_16x16x32_bf16 v[78:81], v[136:139], v[230:233], v[78:81]
	v_mfma_f32_16x16x32_bf16 v[74:77], v[166:169], v[230:233], v[74:77]
	s_setprio 0
	s_setprio 3
	v_mfma_f32_16x16x32_bf16 v[120:123], v[176:179], v[202:205], v[120:123]
	v_mfma_f32_16x16x32_bf16 v[116:119], v[194:197], v[202:205], v[116:119]
	v_mfma_f32_16x16x32_bf16 v[102:105], v[176:179], v[210:213], v[102:105]
	v_mfma_f32_16x16x32_bf16 v[98:101], v[194:197], v[210:213], v[98:101]
	v_mfma_f32_16x16x32_bf16 v[86:89], v[176:179], v[218:221], v[86:89]
	v_mfma_f32_16x16x32_bf16 v[82:85], v[194:197], v[218:221], v[82:85]
	v_mfma_f32_16x16x32_bf16 v[70:73], v[176:179], v[226:229], v[70:73]
	v_mfma_f32_16x16x32_bf16 v[66:69], v[194:197], v[226:229], v[66:69]
	v_mfma_f32_16x16x32_bf16 v[120:123], v[180:183], v[206:209], v[120:123]
	v_mfma_f32_16x16x32_bf16 v[116:119], v[198:201], v[206:209], v[116:119]
	v_mfma_f32_16x16x32_bf16 v[102:105], v[180:183], v[214:217], v[102:105]
	v_mfma_f32_16x16x32_bf16 v[98:101], v[198:201], v[214:217], v[98:101]
	v_mfma_f32_16x16x32_bf16 v[86:89], v[180:183], v[222:225], v[86:89]
	v_mfma_f32_16x16x32_bf16 v[82:85], v[198:201], v[222:225], v[82:85]
	v_mfma_f32_16x16x32_bf16 v[70:73], v[180:183], v[230:233], v[70:73]
	v_mfma_f32_16x16x32_bf16 v[66:69], v[198:201], v[230:233], v[66:69]
	s_setprio 0
	s_barrier
	s_add_u32 s60, s58, 0x8000
	s_addc_u32 s61, s59, 0
	s_add_i32 s16, s16, s4
	v_lshl_add_u64 v[158:159], s[60:61], 0, v[142:143]
	s_mov_b32 m0, s16
	ds_read_b128 v[202:205], v175 offset:49152
	ds_read_b128 v[206:209], v175 offset:50176
	ds_read_b128 v[210:213], v175 offset:51200
	ds_read_b128 v[214:217], v175 offset:52224
	ds_read_b128 v[218:221], v175 offset:53248
	ds_read_b128 v[222:225], v175 offset:54272
	ds_read_b128 v[226:229], v175 offset:55296
	ds_read_b128 v[230:233], v175 offset:56320
	global_load_lds_dwordx4 v[158:159], off
	s_add_i32 m0, s16, 0x2000
	s_add_u32 s58, s58, 0x9000
	v_lshl_add_u64 v[158:159], s[60:61], 0, v[146:147]
	s_addc_u32 s59, s59, 0
	s_add_i32 s16, s17, s4
	global_load_lds_dwordx4 v[158:159], off
	v_lshl_add_u64 v[158:159], s[58:59], 0, v[142:143]
	s_mov_b32 m0, s16
	s_nop 0
	global_load_lds_dwordx4 v[158:159], off
	v_lshl_add_u64 v[158:159], s[58:59], 0, v[146:147]
	s_add_i32 m0, s16, 0x2000
	s_nop 0
	global_load_lds_dwordx4 v[158:159], off
	v_lshl_add_u64 v[158:159], s[56:57], 0, v[140:141]
	s_mov_b32 m0, s62
	s_nop 0
	global_load_lds_dwordx4 v[158:159], off
	v_lshl_add_u64 v[158:159], s[56:57], 0, v[144:145]
	s_mov_b32 m0, s63
	s_nop 0
	global_load_lds_dwordx4 v[158:159], off
	s_waitcnt vmcnt(8)
	s_waitcnt lgkmcnt(0)
	s_barrier
	s_setprio 3
	s_waitcnt lgkmcnt(0)
	v_mfma_f32_16x16x32_bf16 v[62:65], v[132:135], v[202:205], v[62:65]
	v_mfma_f32_16x16x32_bf16 v[58:61], v[152:155], v[202:205], v[58:61]
	v_mfma_f32_16x16x32_bf16 v[46:49], v[132:135], v[210:213], v[46:49]
	v_mfma_f32_16x16x32_bf16 v[42:45], v[152:155], v[210:213], v[42:45]
	v_mfma_f32_16x16x32_bf16 v[30:33], v[132:135], v[218:221], v[30:33]
	v_mfma_f32_16x16x32_bf16 v[26:29], v[152:155], v[218:221], v[26:29]
	v_mfma_f32_16x16x32_bf16 v[14:17], v[132:135], v[226:229], v[14:17]
	v_mfma_f32_16x16x32_bf16 v[10:13], v[152:155], v[226:229], v[10:13]
	v_mfma_f32_16x16x32_bf16 v[62:65], v[136:139], v[206:209], v[62:65]
	v_mfma_f32_16x16x32_bf16 v[58:61], v[166:169], v[206:209], v[58:61]
	v_mfma_f32_16x16x32_bf16 v[46:49], v[136:139], v[214:217], v[46:49]
	v_mfma_f32_16x16x32_bf16 v[42:45], v[166:169], v[214:217], v[42:45]
	v_mfma_f32_16x16x32_bf16 v[30:33], v[136:139], v[222:225], v[30:33]
	v_mfma_f32_16x16x32_bf16 v[26:29], v[166:169], v[222:225], v[26:29]
	v_mfma_f32_16x16x32_bf16 v[14:17], v[136:139], v[230:233], v[14:17]
	v_mfma_f32_16x16x32_bf16 v[10:13], v[166:169], v[230:233], v[10:13]
	s_setprio 0
	s_setprio 3
	v_mfma_f32_16x16x32_bf16 v[54:57], v[176:179], v[202:205], v[54:57]
	v_mfma_f32_16x16x32_bf16 v[50:53], v[194:197], v[202:205], v[50:53]
	v_mfma_f32_16x16x32_bf16 v[38:41], v[176:179], v[210:213], v[38:41]
	v_mfma_f32_16x16x32_bf16 v[34:37], v[194:197], v[210:213], v[34:37]
	v_mfma_f32_16x16x32_bf16 v[22:25], v[176:179], v[218:221], v[22:25]
	v_mfma_f32_16x16x32_bf16 v[18:21], v[194:197], v[218:221], v[18:21]
	v_mfma_f32_16x16x32_bf16 v[6:9], v[176:179], v[226:229], v[6:9]
	v_mfma_f32_16x16x32_bf16 v[2:5], v[194:197], v[226:229], v[2:5]
	v_mfma_f32_16x16x32_bf16 v[54:57], v[180:183], v[206:209], v[54:57]
	v_mfma_f32_16x16x32_bf16 v[50:53], v[198:201], v[206:209], v[50:53]
	v_mfma_f32_16x16x32_bf16 v[38:41], v[180:183], v[214:217], v[38:41]
	v_mfma_f32_16x16x32_bf16 v[34:37], v[198:201], v[214:217], v[34:37]
	v_mfma_f32_16x16x32_bf16 v[22:25], v[180:183], v[222:225], v[22:25]
	v_mfma_f32_16x16x32_bf16 v[18:21], v[198:201], v[222:225], v[18:21]
	v_mfma_f32_16x16x32_bf16 v[6:9], v[180:183], v[230:233], v[6:9]
	v_mfma_f32_16x16x32_bf16 v[2:5], v[198:201], v[230:233], v[2:5]
	s_setprio 0
	s_barrier
	s_add_i32 s67, s67, 2
	s_add_u32 s54, s54, 0x10000
	s_addc_u32 s55, s55, 0
	s_add_u32 s49, s49, 0x10000
	s_addc_u32 s66, s66, 0
	s_cmp_gt_u32 s67, 29
	s_cbranch_scc0 .LBB0_503
	s_add_u32 s100, s29, 0xc000
	s_addc_u32 s101, s15, 0
	v_lshl_add_u64 v[158:159], s[100:101], 0, v[148:149]
	s_add_i32 m0, s12, 0xc000
	s_nop 0
	global_load_lds_dwordx4 v[158:159], off
	v_lshl_add_u64 v[158:159], s[100:101], 0, v[150:151]
	s_add_i32 m0, s12, 0xe000
	s_nop 0
	global_load_lds_dwordx4 v[158:159], off
	s_and_b64 vcc, exec, s[44:45]
	s_cbranch_vccz .LBB0_506
	s_barrier

.LBB0_1079:
	s_add_u32 s16, s52, 0x4000
	s_addc_u32 s17, s53, 0
	s_cmp_eq_u32 s64, 28
	s_cselect_b32 s56, s29, s16
	s_cselect_b32 s57, s24, s17
	s_cselect_b32 s55, s27, s63
	s_cselect_b32 s54, s47, s49
	s_add_u32 s50, s56, 0x8000
	s_addc_u32 s51, s57, 0
	s_add_i32 s16, 0, 0x10000
	v_add_u32_e32 v144, s16, v146
	s_add_i32 s65, 0, 0x14000
	ds_read_b128 v[148:151], v144
	ds_read_b128 v[152:155], v144 offset:1024
	ds_read_b128 v[158:161], v144 offset:2048
	ds_read_b128 v[166:169], v144 offset:3072
	v_add_u32_e32 v144, s65, v146
	ds_read_b128 v[170:173], v144
	ds_read_b128 v[174:177], v144 offset:1024
	ds_read_b128 v[178:181], v144 offset:2048
	ds_read_b128 v[194:197], v144 offset:3072
	v_lshl_add_u64 v[144:145], s[52:53], 0, v[140:141]
	s_add_i32 m0, s20, 0xc000
	ds_read_b128 v[198:201], v147
	ds_read_b128 v[202:205], v147 offset:1024
	ds_read_b128 v[206:209], v147 offset:2048
	ds_read_b128 v[210:213], v147 offset:3072
	ds_read_b128 v[214:217], v147 offset:4096
	ds_read_b128 v[218:221], v147 offset:5120
	ds_read_b128 v[222:225], v147 offset:6144
	ds_read_b128 v[226:229], v147 offset:7168
	global_load_lds_dwordx4 v[144:145], off
	v_lshl_add_u64 v[144:145], s[52:53], 0, v[142:143]
	s_add_i32 m0, s20, 0xe000
	s_nop 0
	global_load_lds_dwordx4 v[144:145], off
	s_waitcnt vmcnt(8)
	s_waitcnt lgkmcnt(0)
	s_barrier
	s_setprio 3
	s_waitcnt lgkmcnt(0)
	v_mfma_f32_16x16x32_bf16 v[116:119], v[148:151], v[198:201], v[116:119]
	v_mfma_f32_16x16x32_bf16 v[124:127], v[158:161], v[198:201], v[124:127]
	v_mfma_f32_16x16x32_bf16 v[98:101], v[148:151], v[206:209], v[98:101]
	v_mfma_f32_16x16x32_bf16 v[102:105], v[158:161], v[206:209], v[102:105]
	v_mfma_f32_16x16x32_bf16 v[82:85], v[148:151], v[214:217], v[82:85]
	v_mfma_f32_16x16x32_bf16 v[90:93], v[158:161], v[214:217], v[90:93]
	v_mfma_f32_16x16x32_bf16 v[58:61], v[148:151], v[222:225], v[58:61]
	v_mfma_f32_16x16x32_bf16 v[70:73], v[158:161], v[222:225], v[70:73]
	v_mfma_f32_16x16x32_bf16 v[116:119], v[152:155], v[202:205], v[116:119]
	v_mfma_f32_16x16x32_bf16 v[124:127], v[166:169], v[202:205], v[124:127]
	v_mfma_f32_16x16x32_bf16 v[98:101], v[152:155], v[210:213], v[98:101]
	v_mfma_f32_16x16x32_bf16 v[102:105], v[166:169], v[210:213], v[102:105]
	v_mfma_f32_16x16x32_bf16 v[82:85], v[152:155], v[218:221], v[82:85]
	v_mfma_f32_16x16x32_bf16 v[90:93], v[166:169], v[218:221], v[90:93]
	v_mfma_f32_16x16x32_bf16 v[58:61], v[152:155], v[226:229], v[58:61]
	v_mfma_f32_16x16x32_bf16 v[70:73], v[166:169], v[226:229], v[70:73]
	s_setprio 0
	s_setprio 3
	v_mfma_f32_16x16x32_bf16 v[120:123], v[170:173], v[198:201], v[120:123]
	v_mfma_f32_16x16x32_bf16 v[128:131], v[178:181], v[198:201], v[128:131]
	v_mfma_f32_16x16x32_bf16 v[106:109], v[170:173], v[206:209], v[106:109]
	v_mfma_f32_16x16x32_bf16 v[110:113], v[178:181], v[206:209], v[110:113]
	v_mfma_f32_16x16x32_bf16 v[86:89], v[170:173], v[214:217], v[86:89]
	v_mfma_f32_16x16x32_bf16 v[94:97], v[178:181], v[214:217], v[94:97]
	v_mfma_f32_16x16x32_bf16 v[74:77], v[170:173], v[222:225], v[74:77]
	v_mfma_f32_16x16x32_bf16 v[78:81], v[178:181], v[222:225], v[78:81]
	v_mfma_f32_16x16x32_bf16 v[120:123], v[174:177], v[202:205], v[120:123]
	v_mfma_f32_16x16x32_bf16 v[128:131], v[194:197], v[202:205], v[128:131]
	v_mfma_f32_16x16x32_bf16 v[106:109], v[174:177], v[210:213], v[106:109]
	v_mfma_f32_16x16x32_bf16 v[110:113], v[194:197], v[210:213], v[110:113]
	v_mfma_f32_16x16x32_bf16 v[86:89], v[174:177], v[218:221], v[86:89]
	v_mfma_f32_16x16x32_bf16 v[94:97], v[194:197], v[218:221], v[94:97]
	v_mfma_f32_16x16x32_bf16 v[74:77], v[174:177], v[226:229], v[74:77]
	v_mfma_f32_16x16x32_bf16 v[78:81], v[194:197], v[226:229], v[78:81]
	s_setprio 0
	s_barrier
	s_add_i32 s16, s16, s13
	v_lshl_add_u64 v[144:145], s[54:55], 0, v[114:115]
	s_mov_b32 m0, s16
	ds_read_b128 v[198:201], v147 offset:16384
	ds_read_b128 v[202:205], v147 offset:17408
	ds_read_b128 v[206:209], v147 offset:18432
	ds_read_b128 v[210:213], v147 offset:19456
	ds_read_b128 v[214:217], v147 offset:20480
	ds_read_b128 v[218:221], v147 offset:21504
	ds_read_b128 v[222:225], v147 offset:22528
	ds_read_b128 v[226:229], v147 offset:23552
	global_load_lds_dwordx4 v[144:145], off
	s_add_i32 m0, s16, 0x2000
	s_add_u32 s16, s54, 0x1000
	v_lshl_add_u64 v[144:145], s[54:55], 0, v[136:137]
	s_addc_u32 s17, s55, 0
	s_add_i32 s65, s65, s13
	global_load_lds_dwordx4 v[144:145], off
	v_lshl_add_u64 v[144:145], s[16:17], 0, v[114:115]
	s_mov_b32 m0, s65
	s_nop 0
	global_load_lds_dwordx4 v[144:145], off
	v_lshl_add_u64 v[144:145], s[16:17], 0, v[136:137]
	s_add_i32 m0, s65, 0x2000
	s_nop 0
	global_load_lds_dwordx4 v[144:145], off
	v_lshl_add_u64 v[144:145], s[56:57], 0, v[132:133]
	s_mov_b32 m0, s20
	s_nop 0
	global_load_lds_dwordx4 v[144:145], off
	v_lshl_add_u64 v[144:145], s[56:57], 0, v[134:135]
	s_mov_b32 m0, s21
	s_nop 0
	global_load_lds_dwordx4 v[144:145], off
	s_waitcnt vmcnt(8)
	s_waitcnt lgkmcnt(0)
	s_barrier
	s_setprio 3
	s_waitcnt lgkmcnt(0)
	v_mfma_f32_16x16x32_bf16 v[50:53], v[148:151], v[198:201], v[50:53]
	v_mfma_f32_16x16x32_bf16 v[62:65], v[158:161], v[198:201], v[62:65]
	v_mfma_f32_16x16x32_bf16 v[34:37], v[148:151], v[206:209], v[34:37]
	v_mfma_f32_16x16x32_bf16 v[38:41], v[158:161], v[206:209], v[38:41]
	v_mfma_f32_16x16x32_bf16 v[18:21], v[148:151], v[214:217], v[18:21]
	v_mfma_f32_16x16x32_bf16 v[26:29], v[158:161], v[214:217], v[26:29]
	v_mfma_f32_16x16x32_bf16 v[2:5], v[148:151], v[222:225], v[2:5]
	v_mfma_f32_16x16x32_bf16 v[6:9], v[158:161], v[222:225], v[6:9]
	v_mfma_f32_16x16x32_bf16 v[50:53], v[152:155], v[202:205], v[50:53]
	v_mfma_f32_16x16x32_bf16 v[62:65], v[166:169], v[202:205], v[62:65]
	v_mfma_f32_16x16x32_bf16 v[34:37], v[152:155], v[210:213], v[34:37]
	v_mfma_f32_16x16x32_bf16 v[38:41], v[166:169], v[210:213], v[38:41]
	v_mfma_f32_16x16x32_bf16 v[18:21], v[152:155], v[218:221], v[18:21]
	v_mfma_f32_16x16x32_bf16 v[26:29], v[166:169], v[218:221], v[26:29]
	v_mfma_f32_16x16x32_bf16 v[2:5], v[152:155], v[226:229], v[2:5]
	v_mfma_f32_16x16x32_bf16 v[6:9], v[166:169], v[226:229], v[6:9]
	s_setprio 0
	s_setprio 3
	v_mfma_f32_16x16x32_bf16 v[54:57], v[170:173], v[198:201], v[54:57]
	v_mfma_f32_16x16x32_bf16 v[66:69], v[178:181], v[198:201], v[66:69]
	v_mfma_f32_16x16x32_bf16 v[42:45], v[170:173], v[206:209], v[42:45]
	v_mfma_f32_16x16x32_bf16 v[46:49], v[178:181], v[206:209], v[46:49]
	v_mfma_f32_16x16x32_bf16 v[22:25], v[170:173], v[214:217], v[22:25]
	v_mfma_f32_16x16x32_bf16 v[30:33], v[178:181], v[214:217], v[30:33]
	v_mfma_f32_16x16x32_bf16 v[10:13], v[170:173], v[222:225], v[10:13]
	v_mfma_f32_16x16x32_bf16 v[14:17], v[178:181], v[222:225], v[14:17]
	v_mfma_f32_16x16x32_bf16 v[54:57], v[174:177], v[202:205], v[54:57]
	v_mfma_f32_16x16x32_bf16 v[66:69], v[194:197], v[202:205], v[66:69]
	v_mfma_f32_16x16x32_bf16 v[42:45], v[174:177], v[210:213], v[42:45]
	v_mfma_f32_16x16x32_bf16 v[46:49], v[194:197], v[210:213], v[46:49]
	v_mfma_f32_16x16x32_bf16 v[22:25], v[174:177], v[218:221], v[22:25]
	v_mfma_f32_16x16x32_bf16 v[30:33], v[194:197], v[218:221], v[30:33]
	v_mfma_f32_16x16x32_bf16 v[10:13], v[174:177], v[226:229], v[10:13]
	v_mfma_f32_16x16x32_bf16 v[14:17], v[194:197], v[226:229], v[14:17]
	s_setprio 0
	s_barrier
	s_add_i32 s65, 0, 0x18000
	v_add_u32_e32 v144, s65, v146
	s_add_i32 s66, 0, 0x1c000
	ds_read_b128 v[148:151], v144
	ds_read_b128 v[152:155], v144 offset:1024
	ds_read_b128 v[158:161], v144 offset:2048
	ds_read_b128 v[166:169], v144 offset:3072
	v_add_u32_e32 v144, s66, v146
	ds_read_b128 v[170:173], v144
	ds_read_b128 v[174:177], v144 offset:1024
	ds_read_b128 v[178:181], v144 offset:2048
	ds_read_b128 v[194:197], v144 offset:3072
	s_add_u32 s16, s56, 0x4000
	s_addc_u32 s17, s57, 0
	s_mov_b32 m0, s37
	v_lshl_add_u64 v[144:145], s[16:17], 0, v[132:133]
	ds_read_b128 v[198:201], v147 offset:32768
	ds_read_b128 v[202:205], v147 offset:33792
	ds_read_b128 v[206:209], v147 offset:34816
	ds_read_b128 v[210:213], v147 offset:35840
	ds_read_b128 v[214:217], v147 offset:36864
	ds_read_b128 v[218:221], v147 offset:37888
	ds_read_b128 v[222:225], v147 offset:38912
	ds_read_b128 v[226:229], v147 offset:39936
	global_load_lds_dwordx4 v[144:145], off
	v_lshl_add_u64 v[144:145], s[16:17], 0, v[134:135]
	s_mov_b32 m0, s58
	s_nop 0
	global_load_lds_dwordx4 v[144:145], off
	s_waitcnt vmcnt(8)
	s_waitcnt lgkmcnt(0)
	s_barrier
	s_setprio 3
	s_waitcnt lgkmcnt(0)
	v_mfma_f32_16x16x32_bf16 v[116:119], v[148:151], v[198:201], v[116:119]
	v_mfma_f32_16x16x32_bf16 v[124:127], v[158:161], v[198:201], v[124:127]
	v_mfma_f32_16x16x32_bf16 v[98:101], v[148:151], v[206:209], v[98:101]
	v_mfma_f32_16x16x32_bf16 v[102:105], v[158:161], v[206:209], v[102:105]
	v_mfma_f32_16x16x32_bf16 v[82:85], v[148:151], v[214:217], v[82:85]
	v_mfma_f32_16x16x32_bf16 v[90:93], v[158:161], v[214:217], v[90:93]
	v_mfma_f32_16x16x32_bf16 v[58:61], v[148:151], v[222:225], v[58:61]
	v_mfma_f32_16x16x32_bf16 v[70:73], v[158:161], v[222:225], v[70:73]
	v_mfma_f32_16x16x32_bf16 v[116:119], v[152:155], v[202:205], v[116:119]
	v_mfma_f32_16x16x32_bf16 v[124:127], v[166:169], v[202:205], v[124:127]
	v_mfma_f32_16x16x32_bf16 v[98:101], v[152:155], v[210:213], v[98:101]
	v_mfma_f32_16x16x32_bf16 v[102:105], v[166:169], v[210:213], v[102:105]
	v_mfma_f32_16x16x32_bf16 v[82:85], v[152:155], v[218:221], v[82:85]
	v_mfma_f32_16x16x32_bf16 v[90:93], v[166:169], v[218:221], v[90:93]
	v_mfma_f32_16x16x32_bf16 v[58:61], v[152:155], v[226:229], v[58:61]
	v_mfma_f32_16x16x32_bf16 v[70:73], v[166:169], v[226:229], v[70:73]
	s_setprio 0
	s_setprio 3
	v_mfma_f32_16x16x32_bf16 v[120:123], v[170:173], v[198:201], v[120:123]
	v_mfma_f32_16x16x32_bf16 v[128:131], v[178:181], v[198:201], v[128:131]
	v_mfma_f32_16x16x32_bf16 v[106:109], v[170:173], v[206:209], v[106:109]
	v_mfma_f32_16x16x32_bf16 v[110:113], v[178:181], v[206:209], v[110:113]
	v_mfma_f32_16x16x32_bf16 v[86:89], v[170:173], v[214:217], v[86:89]
	v_mfma_f32_16x16x32_bf16 v[94:97], v[178:181], v[214:217], v[94:97]
	v_mfma_f32_16x16x32_bf16 v[74:77], v[170:173], v[222:225], v[74:77]
	v_mfma_f32_16x16x32_bf16 v[78:81], v[178:181], v[222:225], v[78:81]
	v_mfma_f32_16x16x32_bf16 v[120:123], v[174:177], v[202:205], v[120:123]
	v_mfma_f32_16x16x32_bf16 v[128:131], v[194:197], v[202:205], v[128:131]
	v_mfma_f32_16x16x32_bf16 v[106:109], v[174:177], v[210:213], v[106:109]
	v_mfma_f32_16x16x32_bf16 v[110:113], v[194:197], v[210:213], v[110:113]
	v_mfma_f32_16x16x32_bf16 v[86:89], v[174:177], v[218:221], v[86:89]
	v_mfma_f32_16x16x32_bf16 v[94:97], v[194:197], v[218:221], v[94:97]
	v_mfma_f32_16x16x32_bf16 v[74:77], v[174:177], v[226:229], v[74:77]
	v_mfma_f32_16x16x32_bf16 v[78:81], v[194:197], v[226:229], v[78:81]
	s_setprio 0
	s_barrier
	s_add_u32 s16, s54, 0x8000
	s_addc_u32 s17, s55, 0
	s_add_i32 s56, s65, s13
	v_lshl_add_u64 v[144:145], s[16:17], 0, v[114:115]
	s_mov_b32 m0, s56
	ds_read_b128 v[198:201], v147 offset:49152
	ds_read_b128 v[202:205], v147 offset:50176
	ds_read_b128 v[206:209], v147 offset:51200
	ds_read_b128 v[210:213], v147 offset:52224
	ds_read_b128 v[214:217], v147 offset:53248
	ds_read_b128 v[218:221], v147 offset:54272
	ds_read_b128 v[222:225], v147 offset:55296
	ds_read_b128 v[226:229], v147 offset:56320
	global_load_lds_dwordx4 v[144:145], off
	s_add_i32 m0, s56, 0x2000
	v_lshl_add_u64 v[144:145], s[16:17], 0, v[136:137]
	s_add_u32 s16, s54, 0x9000
	s_addc_u32 s17, s55, 0
	s_add_i32 s54, s66, s13
	global_load_lds_dwordx4 v[144:145], off
	v_lshl_add_u64 v[144:145], s[16:17], 0, v[114:115]
	s_mov_b32 m0, s54
	s_nop 0
	global_load_lds_dwordx4 v[144:145], off
	v_lshl_add_u64 v[144:145], s[16:17], 0, v[136:137]
	s_add_i32 m0, s54, 0x2000
	s_nop 0
	global_load_lds_dwordx4 v[144:145], off
	v_lshl_add_u64 v[144:145], s[50:51], 0, v[132:133]
	s_mov_b32 m0, s59
	s_nop 0
	global_load_lds_dwordx4 v[144:145], off
	v_lshl_add_u64 v[144:145], s[50:51], 0, v[134:135]
	s_mov_b32 m0, s60
	s_nop 0
	global_load_lds_dwordx4 v[144:145], off
	s_waitcnt vmcnt(8)
	s_waitcnt lgkmcnt(0)
	s_barrier
	s_setprio 3
	s_waitcnt lgkmcnt(0)
	v_mfma_f32_16x16x32_bf16 v[50:53], v[148:151], v[198:201], v[50:53]
	v_mfma_f32_16x16x32_bf16 v[62:65], v[158:161], v[198:201], v[62:65]
	v_mfma_f32_16x16x32_bf16 v[34:37], v[148:151], v[206:209], v[34:37]
	v_mfma_f32_16x16x32_bf16 v[38:41], v[158:161], v[206:209], v[38:41]
	v_mfma_f32_16x16x32_bf16 v[18:21], v[148:151], v[214:217], v[18:21]
	v_mfma_f32_16x16x32_bf16 v[26:29], v[158:161], v[214:217], v[26:29]
	v_mfma_f32_16x16x32_bf16 v[2:5], v[148:151], v[222:225], v[2:5]
	v_mfma_f32_16x16x32_bf16 v[6:9], v[158:161], v[222:225], v[6:9]
	v_mfma_f32_16x16x32_bf16 v[50:53], v[152:155], v[202:205], v[50:53]
	v_mfma_f32_16x16x32_bf16 v[62:65], v[166:169], v[202:205], v[62:65]
	v_mfma_f32_16x16x32_bf16 v[34:37], v[152:155], v[210:213], v[34:37]
	v_mfma_f32_16x16x32_bf16 v[38:41], v[166:169], v[210:213], v[38:41]
	v_mfma_f32_16x16x32_bf16 v[18:21], v[152:155], v[218:221], v[18:21]
	v_mfma_f32_16x16x32_bf16 v[26:29], v[166:169], v[218:221], v[26:29]
	v_mfma_f32_16x16x32_bf16 v[2:5], v[152:155], v[226:229], v[2:5]
	v_mfma_f32_16x16x32_bf16 v[6:9], v[166:169], v[226:229], v[6:9]
	s_setprio 0
	s_setprio 3
	v_mfma_f32_16x16x32_bf16 v[54:57], v[170:173], v[198:201], v[54:57]
	v_mfma_f32_16x16x32_bf16 v[66:69], v[178:181], v[198:201], v[66:69]
	v_mfma_f32_16x16x32_bf16 v[42:45], v[170:173], v[206:209], v[42:45]
	v_mfma_f32_16x16x32_bf16 v[46:49], v[178:181], v[206:209], v[46:49]
	v_mfma_f32_16x16x32_bf16 v[22:25], v[170:173], v[214:217], v[22:25]
	v_mfma_f32_16x16x32_bf16 v[30:33], v[178:181], v[214:217], v[30:33]
	v_mfma_f32_16x16x32_bf16 v[10:13], v[170:173], v[222:225], v[10:13]
	v_mfma_f32_16x16x32_bf16 v[14:17], v[178:181], v[222:225], v[14:17]
	v_mfma_f32_16x16x32_bf16 v[54:57], v[174:177], v[202:205], v[54:57]
	v_mfma_f32_16x16x32_bf16 v[66:69], v[194:197], v[202:205], v[66:69]
	v_mfma_f32_16x16x32_bf16 v[42:45], v[174:177], v[210:213], v[42:45]
	v_mfma_f32_16x16x32_bf16 v[46:49], v[194:197], v[210:213], v[46:49]
	v_mfma_f32_16x16x32_bf16 v[22:25], v[174:177], v[218:221], v[22:25]
	v_mfma_f32_16x16x32_bf16 v[30:33], v[194:197], v[218:221], v[30:33]
	v_mfma_f32_16x16x32_bf16 v[10:13], v[174:177], v[226:229], v[10:13]
	v_mfma_f32_16x16x32_bf16 v[14:17], v[194:197], v[226:229], v[14:17]
	s_setprio 0
	s_barrier
	s_add_i32 s64, s64, 2
	s_add_u32 s52, s52, 0x10000
	s_addc_u32 s53, s53, 0
	s_add_u32 s49, s49, 0x10000
	s_addc_u32 s63, s63, 0
	s_cmp_gt_u32 s64, 29
	s_cbranch_scc0 .LBB0_1079
	s_and_b64 vcc, exec, s[10:11]
	s_cbranch_vccz .LBB0_1082
	s_barrier

.Lrx_relu2_w0:
	s_waitcnt vmcnt(24)
	s_waitcnt lgkmcnt(0)
	s_barrier
	s_setprio 3
	s_waitcnt lgkmcnt(0)
	v_mfma_f32_16x16x32_bf16 v[128:131], v[148:151], v[198:201], v[128:131]
	v_mfma_f32_16x16x32_bf16 v[124:127], v[158:161], v[198:201], v[124:127]
	v_mfma_f32_16x16x32_bf16 v[110:113], v[148:151], v[206:209], v[110:113]
	v_mfma_f32_16x16x32_bf16 v[106:109], v[158:161], v[206:209], v[106:109]
	v_mfma_f32_16x16x32_bf16 v[94:97], v[148:151], v[214:217], v[94:97]
	v_mfma_f32_16x16x32_bf16 v[90:93], v[158:161], v[214:217], v[90:93]
	v_mfma_f32_16x16x32_bf16 v[78:81], v[148:151], v[222:225], v[78:81]
	v_mfma_f32_16x16x32_bf16 v[74:77], v[158:161], v[222:225], v[74:77]
	v_mfma_f32_16x16x32_bf16 v[128:131], v[152:155], v[202:205], v[128:131]
	v_mfma_f32_16x16x32_bf16 v[124:127], v[166:169], v[202:205], v[124:127]
	v_mfma_f32_16x16x32_bf16 v[110:113], v[152:155], v[210:213], v[110:113]
	v_mfma_f32_16x16x32_bf16 v[106:109], v[166:169], v[210:213], v[106:109]
	v_mfma_f32_16x16x32_bf16 v[94:97], v[152:155], v[218:221], v[94:97]
	v_mfma_f32_16x16x32_bf16 v[90:93], v[166:169], v[218:221], v[90:93]
	v_mfma_f32_16x16x32_bf16 v[78:81], v[152:155], v[226:229], v[78:81]
	v_mfma_f32_16x16x32_bf16 v[74:77], v[166:169], v[226:229], v[74:77]
	s_setprio 0
	s_setprio 3
	v_mfma_f32_16x16x32_bf16 v[120:123], v[170:173], v[198:201], v[120:123]
	v_mfma_f32_16x16x32_bf16 v[116:119], v[178:181], v[198:201], v[116:119]
	v_mfma_f32_16x16x32_bf16 v[102:105], v[170:173], v[206:209], v[102:105]
	v_mfma_f32_16x16x32_bf16 v[98:101], v[178:181], v[206:209], v[98:101]
	v_mfma_f32_16x16x32_bf16 v[86:89], v[170:173], v[214:217], v[86:89]
	v_mfma_f32_16x16x32_bf16 v[82:85], v[178:181], v[214:217], v[82:85]
	v_mfma_f32_16x16x32_bf16 v[70:73], v[170:173], v[222:225], v[70:73]
	v_mfma_f32_16x16x32_bf16 v[66:69], v[178:181], v[222:225], v[66:69]
	v_mfma_f32_16x16x32_bf16 v[120:123], v[174:177], v[202:205], v[120:123]
	v_mfma_f32_16x16x32_bf16 v[116:119], v[194:197], v[202:205], v[116:119]
	v_mfma_f32_16x16x32_bf16 v[102:105], v[174:177], v[210:213], v[102:105]
	v_mfma_f32_16x16x32_bf16 v[98:101], v[194:197], v[210:213], v[98:101]
	v_mfma_f32_16x16x32_bf16 v[86:89], v[174:177], v[218:221], v[86:89]
	v_mfma_f32_16x16x32_bf16 v[82:85], v[194:197], v[218:221], v[82:85]
	v_mfma_f32_16x16x32_bf16 v[70:73], v[174:177], v[226:229], v[70:73]
	v_mfma_f32_16x16x32_bf16 v[66:69], v[194:197], v[226:229], v[66:69]
	s_setprio 0
	s_barrier
	s_add_i32 s16, s16, s7
	v_lshl_add_u64 v[144:145], s[50:51], 0, v[114:115]
	s_mov_b32 m0, s16
	ds_read_b128 v[198:201], v147 offset:16384
	ds_read_b128 v[202:205], v147 offset:17408
	ds_read_b128 v[206:209], v147 offset:18432
	ds_read_b128 v[210:213], v147 offset:19456
	ds_read_b128 v[214:217], v147 offset:20480
	ds_read_b128 v[218:221], v147 offset:21504
	ds_read_b128 v[222:225], v147 offset:22528
	ds_read_b128 v[226:229], v147 offset:23552
	global_load_lds_dwordx4 v[144:145], off
	s_add_i32 m0, s16, 0x2000
	s_add_u32 s16, s50, 0x1000
	v_lshl_add_u64 v[144:145], s[50:51], 0, v[136:137]
	s_addc_u32 s17, s51, 0
	s_add_i32 s65, s65, s7
	global_load_lds_dwordx4 v[144:145], off
	v_lshl_add_u64 v[144:145], s[16:17], 0, v[114:115]
	s_mov_b32 m0, s65
	s_nop 0
	global_load_lds_dwordx4 v[144:145], off
	v_lshl_add_u64 v[144:145], s[16:17], 0, v[136:137]
	s_add_i32 m0, s65, 0x2000
	s_nop 0
	global_load_lds_dwordx4 v[144:145], off
	v_lshl_add_u64 v[144:145], s[52:53], 0, v[132:133]
	s_mov_b32 m0, s20
	s_nop 0
	global_load_lds_dwordx4 v[144:145], off
	v_lshl_add_u64 v[144:145], s[52:53], 0, v[134:135]
	s_mov_b32 m0, s21
	s_nop 0
	global_load_lds_dwordx4 v[144:145], off
	s_cmp_lg_u32 s32, 0
	s_cbranch_scc1 .Lrx_relu2_w1
	s_waitcnt vmcnt(8)
.Lrx_relu2_w1:
	s_waitcnt vmcnt(24)
	s_waitcnt lgkmcnt(0)
	s_barrier
	s_setprio 3
	s_waitcnt lgkmcnt(0)
	v_mfma_f32_16x16x32_bf16 v[62:65], v[148:151], v[198:201], v[62:65]
	v_mfma_f32_16x16x32_bf16 v[58:61], v[158:161], v[198:201], v[58:61]
	v_mfma_f32_16x16x32_bf16 v[46:49], v[148:151], v[206:209], v[46:49]
	v_mfma_f32_16x16x32_bf16 v[42:45], v[158:161], v[206:209], v[42:45]
	v_mfma_f32_16x16x32_bf16 v[30:33], v[148:151], v[214:217], v[30:33]
	v_mfma_f32_16x16x32_bf16 v[26:29], v[158:161], v[214:217], v[26:29]
	v_mfma_f32_16x16x32_bf16 v[14:17], v[148:151], v[222:225], v[14:17]
	v_mfma_f32_16x16x32_bf16 v[10:13], v[158:161], v[222:225], v[10:13]
	v_mfma_f32_16x16x32_bf16 v[62:65], v[152:155], v[202:205], v[62:65]
	v_mfma_f32_16x16x32_bf16 v[58:61], v[166:169], v[202:205], v[58:61]
	v_mfma_f32_16x16x32_bf16 v[46:49], v[152:155], v[210:213], v[46:49]
	v_mfma_f32_16x16x32_bf16 v[42:45], v[166:169], v[210:213], v[42:45]
	v_mfma_f32_16x16x32_bf16 v[30:33], v[152:155], v[218:221], v[30:33]
	v_mfma_f32_16x16x32_bf16 v[26:29], v[166:169], v[218:221], v[26:29]
	v_mfma_f32_16x16x32_bf16 v[14:17], v[152:155], v[226:229], v[14:17]
	v_mfma_f32_16x16x32_bf16 v[10:13], v[166:169], v[226:229], v[10:13]
	s_setprio 0
	s_setprio 3
	v_mfma_f32_16x16x32_bf16 v[54:57], v[170:173], v[198:201], v[54:57]
	v_mfma_f32_16x16x32_bf16 v[50:53], v[178:181], v[198:201], v[50:53]
	v_mfma_f32_16x16x32_bf16 v[38:41], v[170:173], v[206:209], v[38:41]
	v_mfma_f32_16x16x32_bf16 v[34:37], v[178:181], v[206:209], v[34:37]
	v_mfma_f32_16x16x32_bf16 v[22:25], v[170:173], v[214:217], v[22:25]
	v_mfma_f32_16x16x32_bf16 v[18:21], v[178:181], v[214:217], v[18:21]
	v_mfma_f32_16x16x32_bf16 v[6:9], v[170:173], v[222:225], v[6:9]
	v_mfma_f32_16x16x32_bf16 v[2:5], v[178:181], v[222:225], v[2:5]
	v_mfma_f32_16x16x32_bf16 v[54:57], v[174:177], v[202:205], v[54:57]
	v_mfma_f32_16x16x32_bf16 v[50:53], v[194:197], v[202:205], v[50:53]
	v_mfma_f32_16x16x32_bf16 v[38:41], v[174:177], v[210:213], v[38:41]
	v_mfma_f32_16x16x32_bf16 v[34:37], v[194:197], v[210:213], v[34:37]
	v_mfma_f32_16x16x32_bf16 v[22:25], v[174:177], v[218:221], v[22:25]
	v_mfma_f32_16x16x32_bf16 v[18:21], v[194:197], v[218:221], v[18:21]
	v_mfma_f32_16x16x32_bf16 v[6:9], v[174:177], v[226:229], v[6:9]
	v_mfma_f32_16x16x32_bf16 v[2:5], v[194:197], v[226:229], v[2:5]
	s_setprio 0
	s_barrier
	s_add_i32 s65, 0, 0x18000
	v_add_u32_e32 v144, s65, v1
	s_add_i32 s66, 0, 0x1c000
	ds_read_b128 v[148:151], v144
	ds_read_b128 v[152:155], v144 offset:1024
	ds_read_b128 v[158:161], v144 offset:2048
	ds_read_b128 v[166:169], v144 offset:3072
	v_add_u32_e32 v144, s66, v1
	ds_read_b128 v[170:173], v144
	ds_read_b128 v[174:177], v144 offset:1024
	ds_read_b128 v[178:181], v144 offset:2048
	ds_read_b128 v[194:197], v144 offset:3072
	s_add_u32 s16, s52, 0x4000
	s_addc_u32 s17, s53, 0
	s_mov_b32 m0, s24
	v_lshl_add_u64 v[144:145], s[16:17], 0, v[132:133]
	ds_read_b128 v[198:201], v147 offset:32768
	ds_read_b128 v[202:205], v147 offset:33792
	ds_read_b128 v[206:209], v147 offset:34816
	ds_read_b128 v[210:213], v147 offset:35840
	ds_read_b128 v[214:217], v147 offset:36864
	ds_read_b128 v[218:221], v147 offset:37888
	ds_read_b128 v[222:225], v147 offset:38912
	ds_read_b128 v[226:229], v147 offset:39936
	global_load_lds_dwordx4 v[144:145], off
	v_lshl_add_u64 v[144:145], s[16:17], 0, v[134:135]
	s_mov_b32 m0, s37
	s_nop 0
	global_load_lds_dwordx4 v[144:145], off
	s_cmp_lg_u32 s32, 0
	s_cbranch_scc1 .Lrx_relu2_w2
	s_waitcnt vmcnt(8)
.Lrx_relu2_w2:
	s_waitcnt vmcnt(24)
	s_mov_b32 s32, 0
	s_waitcnt lgkmcnt(0)
	s_barrier
	s_setprio 3
	s_waitcnt lgkmcnt(0)
	v_mfma_f32_16x16x32_bf16 v[128:131], v[148:151], v[198:201], v[128:131]
	v_mfma_f32_16x16x32_bf16 v[124:127], v[158:161], v[198:201], v[124:127]
	v_mfma_f32_16x16x32_bf16 v[110:113], v[148:151], v[206:209], v[110:113]
	v_mfma_f32_16x16x32_bf16 v[106:109], v[158:161], v[206:209], v[106:109]
	v_mfma_f32_16x16x32_bf16 v[94:97], v[148:151], v[214:217], v[94:97]
	v_mfma_f32_16x16x32_bf16 v[90:93], v[158:161], v[214:217], v[90:93]
	v_mfma_f32_16x16x32_bf16 v[78:81], v[148:151], v[222:225], v[78:81]
	v_mfma_f32_16x16x32_bf16 v[74:77], v[158:161], v[222:225], v[74:77]
	v_mfma_f32_16x16x32_bf16 v[128:131], v[152:155], v[202:205], v[128:131]
	v_mfma_f32_16x16x32_bf16 v[124:127], v[166:169], v[202:205], v[124:127]
	v_mfma_f32_16x16x32_bf16 v[110:113], v[152:155], v[210:213], v[110:113]
	v_mfma_f32_16x16x32_bf16 v[106:109], v[166:169], v[210:213], v[106:109]
	v_mfma_f32_16x16x32_bf16 v[94:97], v[152:155], v[218:221], v[94:97]
	v_mfma_f32_16x16x32_bf16 v[90:93], v[166:169], v[218:221], v[90:93]
	v_mfma_f32_16x16x32_bf16 v[78:81], v[152:155], v[226:229], v[78:81]
	v_mfma_f32_16x16x32_bf16 v[74:77], v[166:169], v[226:229], v[74:77]
	s_setprio 0
	s_setprio 3
	v_mfma_f32_16x16x32_bf16 v[120:123], v[170:173], v[198:201], v[120:123]
	v_mfma_f32_16x16x32_bf16 v[116:119], v[178:181], v[198:201], v[116:119]
	v_mfma_f32_16x16x32_bf16 v[102:105], v[170:173], v[206:209], v[102:105]
	v_mfma_f32_16x16x32_bf16 v[98:101], v[178:181], v[206:209], v[98:101]
	v_mfma_f32_16x16x32_bf16 v[86:89], v[170:173], v[214:217], v[86:89]
	v_mfma_f32_16x16x32_bf16 v[82:85], v[178:181], v[214:217], v[82:85]
	v_mfma_f32_16x16x32_bf16 v[70:73], v[170:173], v[222:225], v[70:73]
	v_mfma_f32_16x16x32_bf16 v[66:69], v[178:181], v[222:225], v[66:69]
	v_mfma_f32_16x16x32_bf16 v[120:123], v[174:177], v[202:205], v[120:123]
	v_mfma_f32_16x16x32_bf16 v[116:119], v[194:197], v[202:205], v[116:119]
	v_mfma_f32_16x16x32_bf16 v[102:105], v[174:177], v[210:213], v[102:105]
	v_mfma_f32_16x16x32_bf16 v[98:101], v[194:197], v[210:213], v[98:101]
	v_mfma_f32_16x16x32_bf16 v[86:89], v[174:177], v[218:221], v[86:89]
	v_mfma_f32_16x16x32_bf16 v[82:85], v[194:197], v[218:221], v[82:85]
	v_mfma_f32_16x16x32_bf16 v[70:73], v[174:177], v[226:229], v[70:73]
	v_mfma_f32_16x16x32_bf16 v[66:69], v[194:197], v[226:229], v[66:69]
	s_setprio 0
	s_barrier
	s_add_u32 s16, s50, 0x8000
	s_addc_u32 s17, s51, 0
	s_add_i32 s52, s65, s7
	v_lshl_add_u64 v[144:145], s[16:17], 0, v[114:115]
	s_mov_b32 m0, s52
	ds_read_b128 v[198:201], v147 offset:49152
	ds_read_b128 v[202:205], v147 offset:50176
	ds_read_b128 v[206:209], v147 offset:51200
	ds_read_b128 v[210:213], v147 offset:52224
	ds_read_b128 v[214:217], v147 offset:53248
	ds_read_b128 v[218:221], v147 offset:54272
	ds_read_b128 v[222:225], v147 offset:55296
	ds_read_b128 v[226:229], v147 offset:56320
	global_load_lds_dwordx4 v[144:145], off
	s_add_i32 m0, s52, 0x2000
	v_lshl_add_u64 v[144:145], s[16:17], 0, v[136:137]
	s_add_u32 s16, s50, 0x9000
	s_addc_u32 s17, s51, 0
	s_add_i32 s50, s66, s7
	global_load_lds_dwordx4 v[144:145], off
	v_lshl_add_u64 v[144:145], s[16:17], 0, v[114:115]
	s_mov_b32 m0, s50
	s_nop 0
	global_load_lds_dwordx4 v[144:145], off
	v_lshl_add_u64 v[144:145], s[16:17], 0, v[136:137]
	s_add_i32 m0, s50, 0x2000
	s_nop 0
	global_load_lds_dwordx4 v[144:145], off
	v_lshl_add_u64 v[144:145], s[48:49], 0, v[132:133]
	s_mov_b32 m0, s54
	s_nop 0
	global_load_lds_dwordx4 v[144:145], off
	v_lshl_add_u64 v[144:145], s[48:49], 0, v[134:135]
	s_mov_b32 m0, s55
	s_nop 0
	global_load_lds_dwordx4 v[144:145], off
	s_waitcnt vmcnt(8)
	s_waitcnt lgkmcnt(0)
	s_barrier
	s_setprio 3
	s_waitcnt lgkmcnt(0)
	v_mfma_f32_16x16x32_bf16 v[62:65], v[148:151], v[198:201], v[62:65]
	v_mfma_f32_16x16x32_bf16 v[58:61], v[158:161], v[198:201], v[58:61]
	v_mfma_f32_16x16x32_bf16 v[46:49], v[148:151], v[206:209], v[46:49]
	v_mfma_f32_16x16x32_bf16 v[42:45], v[158:161], v[206:209], v[42:45]
	v_mfma_f32_16x16x32_bf16 v[30:33], v[148:151], v[214:217], v[30:33]
	v_mfma_f32_16x16x32_bf16 v[26:29], v[158:161], v[214:217], v[26:29]
	v_mfma_f32_16x16x32_bf16 v[14:17], v[148:151], v[222:225], v[14:17]
	v_mfma_f32_16x16x32_bf16 v[10:13], v[158:161], v[222:225], v[10:13]
	v_mfma_f32_16x16x32_bf16 v[62:65], v[152:155], v[202:205], v[62:65]
	v_mfma_f32_16x16x32_bf16 v[58:61], v[166:169], v[202:205], v[58:61]
	v_mfma_f32_16x16x32_bf16 v[46:49], v[152:155], v[210:213], v[46:49]
	v_mfma_f32_16x16x32_bf16 v[42:45], v[166:169], v[210:213], v[42:45]
	v_mfma_f32_16x16x32_bf16 v[30:33], v[152:155], v[218:221], v[30:33]
	v_mfma_f32_16x16x32_bf16 v[26:29], v[166:169], v[218:221], v[26:29]
	v_mfma_f32_16x16x32_bf16 v[14:17], v[152:155], v[226:229], v[14:17]
	v_mfma_f32_16x16x32_bf16 v[10:13], v[166:169], v[226:229], v[10:13]
	s_setprio 0
	s_setprio 3
	v_mfma_f32_16x16x32_bf16 v[54:57], v[170:173], v[198:201], v[54:57]
	v_mfma_f32_16x16x32_bf16 v[50:53], v[178:181], v[198:201], v[50:53]
	v_mfma_f32_16x16x32_bf16 v[38:41], v[170:173], v[206:209], v[38:41]
	v_mfma_f32_16x16x32_bf16 v[34:37], v[178:181], v[206:209], v[34:37]
	v_mfma_f32_16x16x32_bf16 v[22:25], v[170:173], v[214:217], v[22:25]
	v_mfma_f32_16x16x32_bf16 v[18:21], v[178:181], v[214:217], v[18:21]
	v_mfma_f32_16x16x32_bf16 v[6:9], v[170:173], v[222:225], v[6:9]
	v_mfma_f32_16x16x32_bf16 v[2:5], v[178:181], v[222:225], v[2:5]
	v_mfma_f32_16x16x32_bf16 v[54:57], v[174:177], v[202:205], v[54:57]
	v_mfma_f32_16x16x32_bf16 v[50:53], v[194:197], v[202:205], v[50:53]
	v_mfma_f32_16x16x32_bf16 v[38:41], v[174:177], v[210:213], v[38:41]
	v_mfma_f32_16x16x32_bf16 v[34:37], v[194:197], v[210:213], v[34:37]
	v_mfma_f32_16x16x32_bf16 v[22:25], v[174:177], v[218:221], v[22:25]
	v_mfma_f32_16x16x32_bf16 v[18:21], v[194:197], v[218:221], v[18:21]
	v_mfma_f32_16x16x32_bf16 v[6:9], v[174:177], v[226:229], v[6:9]
	v_mfma_f32_16x16x32_bf16 v[2:5], v[194:197], v[226:229], v[2:5]
	s_setprio 0
	s_barrier
	s_add_i32 s64, s64, 2
	s_add_u32 s46, s46, 0x10000
	s_addc_u32 s47, s47, 0
	s_add_u32 s62, s62, 0x10000
	s_addc_u32 s63, s63, 0
	s_cmp_gt_u32 s64, 29
	s_cbranch_scc0 .LBB0_1230
	s_add_u32 s100, s60, 0xc000
	s_addc_u32 s101, s29, 0
	v_lshl_add_u64 v[144:145], s[100:101], 0, v[140:141]
	s_add_i32 m0, s20, 0xc000
	s_nop 0
	global_load_lds_dwordx4 v[144:145], off
	v_lshl_add_u64 v[144:145], s[100:101], 0, v[142:143]
	s_add_i32 m0, s20, 0xe000
	s_nop 0
	global_load_lds_dwordx4 v[144:145], off
	s_and_b64 vcc, exec, s[10:11]
	s_cbranch_vccz .LBB0_1233
	s_barrier

.LBB0_1334:
	s_add_u32 s16, s52, 0x4000
	s_addc_u32 s17, s53, 0
	s_cmpk_eq_i32 s66, 0x7c
	s_cselect_b32 s56, s29, s16
	s_cselect_b32 s57, s24, s17
	s_cselect_b32 s55, s27, s65
	s_cselect_b32 s54, s47, s49
	s_add_u32 s50, s56, 0x8000
	s_addc_u32 s51, s57, 0
	s_add_i32 s16, 0, 0x10000
	v_add_u32_e32 v144, s16, v146
	s_add_i32 s67, 0, 0x14000
	ds_read_b128 v[148:151], v144
	ds_read_b128 v[152:155], v144 offset:1024
	ds_read_b128 v[158:161], v144 offset:2048
	ds_read_b128 v[166:169], v144 offset:3072
	v_add_u32_e32 v144, s67, v146
	ds_read_b128 v[170:173], v144
	ds_read_b128 v[174:177], v144 offset:1024
	ds_read_b128 v[178:181], v144 offset:2048
	ds_read_b128 v[194:197], v144 offset:3072
	v_lshl_add_u64 v[144:145], s[52:53], 0, v[140:141]
	s_add_i32 m0, s37, 0xc000
	ds_read_b128 v[198:201], v147
	ds_read_b128 v[202:205], v147 offset:1024
	ds_read_b128 v[206:209], v147 offset:2048
	ds_read_b128 v[210:213], v147 offset:3072
	ds_read_b128 v[214:217], v147 offset:4096
	ds_read_b128 v[218:221], v147 offset:5120
	ds_read_b128 v[222:225], v147 offset:6144
	ds_read_b128 v[226:229], v147 offset:7168
	global_load_lds_dwordx4 v[144:145], off
	v_lshl_add_u64 v[144:145], s[52:53], 0, v[142:143]
	s_add_i32 m0, s37, 0xe000
	s_nop 0
	global_load_lds_dwordx4 v[144:145], off
	s_waitcnt vmcnt(8)
	s_waitcnt lgkmcnt(0)
	s_barrier
	s_setprio 3
	s_waitcnt lgkmcnt(0)
	v_mfma_f32_16x16x32_bf16 v[116:119], v[148:151], v[198:201], v[116:119]
	v_mfma_f32_16x16x32_bf16 v[124:127], v[158:161], v[198:201], v[124:127]
	v_mfma_f32_16x16x32_bf16 v[98:101], v[148:151], v[206:209], v[98:101]
	v_mfma_f32_16x16x32_bf16 v[102:105], v[158:161], v[206:209], v[102:105]
	v_mfma_f32_16x16x32_bf16 v[82:85], v[148:151], v[214:217], v[82:85]
	v_mfma_f32_16x16x32_bf16 v[90:93], v[158:161], v[214:217], v[90:93]
	v_mfma_f32_16x16x32_bf16 v[58:61], v[148:151], v[222:225], v[58:61]
	v_mfma_f32_16x16x32_bf16 v[70:73], v[158:161], v[222:225], v[70:73]
	v_mfma_f32_16x16x32_bf16 v[116:119], v[152:155], v[202:205], v[116:119]
	v_mfma_f32_16x16x32_bf16 v[124:127], v[166:169], v[202:205], v[124:127]
	v_mfma_f32_16x16x32_bf16 v[98:101], v[152:155], v[210:213], v[98:101]
	v_mfma_f32_16x16x32_bf16 v[102:105], v[166:169], v[210:213], v[102:105]
	v_mfma_f32_16x16x32_bf16 v[82:85], v[152:155], v[218:221], v[82:85]
	v_mfma_f32_16x16x32_bf16 v[90:93], v[166:169], v[218:221], v[90:93]
	v_mfma_f32_16x16x32_bf16 v[58:61], v[152:155], v[226:229], v[58:61]
	v_mfma_f32_16x16x32_bf16 v[70:73], v[166:169], v[226:229], v[70:73]
	s_setprio 0
	s_setprio 3
	v_mfma_f32_16x16x32_bf16 v[120:123], v[170:173], v[198:201], v[120:123]
	v_mfma_f32_16x16x32_bf16 v[128:131], v[178:181], v[198:201], v[128:131]
	v_mfma_f32_16x16x32_bf16 v[106:109], v[170:173], v[206:209], v[106:109]
	v_mfma_f32_16x16x32_bf16 v[110:113], v[178:181], v[206:209], v[110:113]
	v_mfma_f32_16x16x32_bf16 v[86:89], v[170:173], v[214:217], v[86:89]
	v_mfma_f32_16x16x32_bf16 v[94:97], v[178:181], v[214:217], v[94:97]
	v_mfma_f32_16x16x32_bf16 v[74:77], v[170:173], v[222:225], v[74:77]
	v_mfma_f32_16x16x32_bf16 v[78:81], v[178:181], v[222:225], v[78:81]
	v_mfma_f32_16x16x32_bf16 v[120:123], v[174:177], v[202:205], v[120:123]
	v_mfma_f32_16x16x32_bf16 v[128:131], v[194:197], v[202:205], v[128:131]
	v_mfma_f32_16x16x32_bf16 v[106:109], v[174:177], v[210:213], v[106:109]
	v_mfma_f32_16x16x32_bf16 v[110:113], v[194:197], v[210:213], v[110:113]
	v_mfma_f32_16x16x32_bf16 v[86:89], v[174:177], v[218:221], v[86:89]
	v_mfma_f32_16x16x32_bf16 v[94:97], v[194:197], v[218:221], v[94:97]
	v_mfma_f32_16x16x32_bf16 v[74:77], v[174:177], v[226:229], v[74:77]
	v_mfma_f32_16x16x32_bf16 v[78:81], v[194:197], v[226:229], v[78:81]
	s_setprio 0
	s_barrier
	s_add_i32 s16, s16, s15
	v_lshl_add_u64 v[144:145], s[54:55], 0, v[114:115]
	s_mov_b32 m0, s16
	ds_read_b128 v[198:201], v147 offset:16384
	ds_read_b128 v[202:205], v147 offset:17408
	ds_read_b128 v[206:209], v147 offset:18432
	ds_read_b128 v[210:213], v147 offset:19456
	ds_read_b128 v[214:217], v147 offset:20480
	ds_read_b128 v[218:221], v147 offset:21504
	ds_read_b128 v[222:225], v147 offset:22528
	ds_read_b128 v[226:229], v147 offset:23552
	global_load_lds_dwordx4 v[144:145], off
	s_add_i32 m0, s16, 0x2000
	s_add_u32 s16, s54, 0x1000
	v_lshl_add_u64 v[144:145], s[54:55], 0, v[136:137]
	s_addc_u32 s17, s55, 0
	s_add_i32 s67, s67, s15
	global_load_lds_dwordx4 v[144:145], off
	v_lshl_add_u64 v[144:145], s[16:17], 0, v[114:115]
	s_mov_b32 m0, s67
	s_nop 0
	global_load_lds_dwordx4 v[144:145], off
	v_lshl_add_u64 v[144:145], s[16:17], 0, v[136:137]
	s_add_i32 m0, s67, 0x2000
	s_nop 0
	global_load_lds_dwordx4 v[144:145], off
	v_lshl_add_u64 v[144:145], s[56:57], 0, v[132:133]
	s_mov_b32 m0, s37
	s_nop 0
	global_load_lds_dwordx4 v[144:145], off
	v_lshl_add_u64 v[144:145], s[56:57], 0, v[134:135]
	s_mov_b32 m0, s58
	s_nop 0
	global_load_lds_dwordx4 v[144:145], off
	s_waitcnt vmcnt(8)
	s_waitcnt lgkmcnt(0)
	s_barrier
	s_setprio 3
	s_waitcnt lgkmcnt(0)
	v_mfma_f32_16x16x32_bf16 v[50:53], v[148:151], v[198:201], v[50:53]
	v_mfma_f32_16x16x32_bf16 v[62:65], v[158:161], v[198:201], v[62:65]
	v_mfma_f32_16x16x32_bf16 v[34:37], v[148:151], v[206:209], v[34:37]
	v_mfma_f32_16x16x32_bf16 v[38:41], v[158:161], v[206:209], v[38:41]
	v_mfma_f32_16x16x32_bf16 v[18:21], v[148:151], v[214:217], v[18:21]
	v_mfma_f32_16x16x32_bf16 v[26:29], v[158:161], v[214:217], v[26:29]
	v_mfma_f32_16x16x32_bf16 v[2:5], v[148:151], v[222:225], v[2:5]
	v_mfma_f32_16x16x32_bf16 v[6:9], v[158:161], v[222:225], v[6:9]
	v_mfma_f32_16x16x32_bf16 v[50:53], v[152:155], v[202:205], v[50:53]
	v_mfma_f32_16x16x32_bf16 v[62:65], v[166:169], v[202:205], v[62:65]
	v_mfma_f32_16x16x32_bf16 v[34:37], v[152:155], v[210:213], v[34:37]
	v_mfma_f32_16x16x32_bf16 v[38:41], v[166:169], v[210:213], v[38:41]
	v_mfma_f32_16x16x32_bf16 v[18:21], v[152:155], v[218:221], v[18:21]
	v_mfma_f32_16x16x32_bf16 v[26:29], v[166:169], v[218:221], v[26:29]
	v_mfma_f32_16x16x32_bf16 v[2:5], v[152:155], v[226:229], v[2:5]
	v_mfma_f32_16x16x32_bf16 v[6:9], v[166:169], v[226:229], v[6:9]
	s_setprio 0
	s_setprio 3
	v_mfma_f32_16x16x32_bf16 v[54:57], v[170:173], v[198:201], v[54:57]
	v_mfma_f32_16x16x32_bf16 v[66:69], v[178:181], v[198:201], v[66:69]
	v_mfma_f32_16x16x32_bf16 v[42:45], v[170:173], v[206:209], v[42:45]
	v_mfma_f32_16x16x32_bf16 v[46:49], v[178:181], v[206:209], v[46:49]
	v_mfma_f32_16x16x32_bf16 v[22:25], v[170:173], v[214:217], v[22:25]
	v_mfma_f32_16x16x32_bf16 v[30:33], v[178:181], v[214:217], v[30:33]
	v_mfma_f32_16x16x32_bf16 v[10:13], v[170:173], v[222:225], v[10:13]
	v_mfma_f32_16x16x32_bf16 v[14:17], v[178:181], v[222:225], v[14:17]
	v_mfma_f32_16x16x32_bf16 v[54:57], v[174:177], v[202:205], v[54:57]
	v_mfma_f32_16x16x32_bf16 v[66:69], v[194:197], v[202:205], v[66:69]
	v_mfma_f32_16x16x32_bf16 v[42:45], v[174:177], v[210:213], v[42:45]
	v_mfma_f32_16x16x32_bf16 v[46:49], v[194:197], v[210:213], v[46:49]
	v_mfma_f32_16x16x32_bf16 v[22:25], v[174:177], v[218:221], v[22:25]
	v_mfma_f32_16x16x32_bf16 v[30:33], v[194:197], v[218:221], v[30:33]
	v_mfma_f32_16x16x32_bf16 v[10:13], v[174:177], v[226:229], v[10:13]
	v_mfma_f32_16x16x32_bf16 v[14:17], v[194:197], v[226:229], v[14:17]
	s_setprio 0
	s_barrier
	s_add_i32 s67, 0, 0x18000
	v_add_u32_e32 v144, s67, v146
	s_add_i32 s68, 0, 0x1c000
	ds_read_b128 v[148:151], v144
	ds_read_b128 v[152:155], v144 offset:1024
	ds_read_b128 v[158:161], v144 offset:2048
	ds_read_b128 v[166:169], v144 offset:3072
	v_add_u32_e32 v144, s68, v146
	ds_read_b128 v[170:173], v144
	ds_read_b128 v[174:177], v144 offset:1024
	ds_read_b128 v[178:181], v144 offset:2048
	ds_read_b128 v[194:197], v144 offset:3072
	s_add_u32 s16, s56, 0x4000
	s_addc_u32 s17, s57, 0
	s_mov_b32 m0, s59
	v_lshl_add_u64 v[144:145], s[16:17], 0, v[132:133]
	ds_read_b128 v[198:201], v147 offset:32768
	ds_read_b128 v[202:205], v147 offset:33792
	ds_read_b128 v[206:209], v147 offset:34816
	ds_read_b128 v[210:213], v147 offset:35840
	ds_read_b128 v[214:217], v147 offset:36864
	ds_read_b128 v[218:221], v147 offset:37888
	ds_read_b128 v[222:225], v147 offset:38912
	ds_read_b128 v[226:229], v147 offset:39936
	global_load_lds_dwordx4 v[144:145], off
	v_lshl_add_u64 v[144:145], s[16:17], 0, v[134:135]
	s_mov_b32 m0, s60
	s_nop 0
	global_load_lds_dwordx4 v[144:145], off
	s_waitcnt vmcnt(8)
	s_waitcnt lgkmcnt(0)
	s_barrier
	s_setprio 3
	s_waitcnt lgkmcnt(0)
	v_mfma_f32_16x16x32_bf16 v[116:119], v[148:151], v[198:201], v[116:119]
	v_mfma_f32_16x16x32_bf16 v[124:127], v[158:161], v[198:201], v[124:127]
	v_mfma_f32_16x16x32_bf16 v[98:101], v[148:151], v[206:209], v[98:101]
	v_mfma_f32_16x16x32_bf16 v[102:105], v[158:161], v[206:209], v[102:105]
	v_mfma_f32_16x16x32_bf16 v[82:85], v[148:151], v[214:217], v[82:85]
	v_mfma_f32_16x16x32_bf16 v[90:93], v[158:161], v[214:217], v[90:93]
	v_mfma_f32_16x16x32_bf16 v[58:61], v[148:151], v[222:225], v[58:61]
	v_mfma_f32_16x16x32_bf16 v[70:73], v[158:161], v[222:225], v[70:73]
	v_mfma_f32_16x16x32_bf16 v[116:119], v[152:155], v[202:205], v[116:119]
	v_mfma_f32_16x16x32_bf16 v[124:127], v[166:169], v[202:205], v[124:127]
	v_mfma_f32_16x16x32_bf16 v[98:101], v[152:155], v[210:213], v[98:101]
	v_mfma_f32_16x16x32_bf16 v[102:105], v[166:169], v[210:213], v[102:105]
	v_mfma_f32_16x16x32_bf16 v[82:85], v[152:155], v[218:221], v[82:85]
	v_mfma_f32_16x16x32_bf16 v[90:93], v[166:169], v[218:221], v[90:93]
	v_mfma_f32_16x16x32_bf16 v[58:61], v[152:155], v[226:229], v[58:61]
	v_mfma_f32_16x16x32_bf16 v[70:73], v[166:169], v[226:229], v[70:73]
	s_setprio 0
	s_setprio 3
	v_mfma_f32_16x16x32_bf16 v[120:123], v[170:173], v[198:201], v[120:123]
	v_mfma_f32_16x16x32_bf16 v[128:131], v[178:181], v[198:201], v[128:131]
	v_mfma_f32_16x16x32_bf16 v[106:109], v[170:173], v[206:209], v[106:109]
	v_mfma_f32_16x16x32_bf16 v[110:113], v[178:181], v[206:209], v[110:113]
	v_mfma_f32_16x16x32_bf16 v[86:89], v[170:173], v[214:217], v[86:89]
	v_mfma_f32_16x16x32_bf16 v[94:97], v[178:181], v[214:217], v[94:97]
	v_mfma_f32_16x16x32_bf16 v[74:77], v[170:173], v[222:225], v[74:77]
	v_mfma_f32_16x16x32_bf16 v[78:81], v[178:181], v[222:225], v[78:81]
	v_mfma_f32_16x16x32_bf16 v[120:123], v[174:177], v[202:205], v[120:123]
	v_mfma_f32_16x16x32_bf16 v[128:131], v[194:197], v[202:205], v[128:131]
	v_mfma_f32_16x16x32_bf16 v[106:109], v[174:177], v[210:213], v[106:109]
	v_mfma_f32_16x16x32_bf16 v[110:113], v[194:197], v[210:213], v[110:113]
	v_mfma_f32_16x16x32_bf16 v[86:89], v[174:177], v[218:221], v[86:89]
	v_mfma_f32_16x16x32_bf16 v[94:97], v[194:197], v[218:221], v[94:97]
	v_mfma_f32_16x16x32_bf16 v[74:77], v[174:177], v[226:229], v[74:77]
	v_mfma_f32_16x16x32_bf16 v[78:81], v[194:197], v[226:229], v[78:81]
	s_setprio 0
	s_barrier
	s_add_u32 s16, s54, 0x8000
	s_addc_u32 s17, s55, 0
	s_add_i32 s56, s67, s15
	v_lshl_add_u64 v[144:145], s[16:17], 0, v[114:115]
	s_mov_b32 m0, s56
	ds_read_b128 v[198:201], v147 offset:49152
	ds_read_b128 v[202:205], v147 offset:50176
	ds_read_b128 v[206:209], v147 offset:51200
	ds_read_b128 v[210:213], v147 offset:52224
	ds_read_b128 v[214:217], v147 offset:53248
	ds_read_b128 v[218:221], v147 offset:54272
	ds_read_b128 v[222:225], v147 offset:55296
	ds_read_b128 v[226:229], v147 offset:56320
	global_load_lds_dwordx4 v[144:145], off
	s_add_i32 m0, s56, 0x2000
	v_lshl_add_u64 v[144:145], s[16:17], 0, v[136:137]
	s_add_u32 s16, s54, 0x9000
	s_addc_u32 s17, s55, 0
	s_add_i32 s54, s68, s15
	global_load_lds_dwordx4 v[144:145], off
	v_lshl_add_u64 v[144:145], s[16:17], 0, v[114:115]
	s_mov_b32 m0, s54
	s_nop 0
	global_load_lds_dwordx4 v[144:145], off
	v_lshl_add_u64 v[144:145], s[16:17], 0, v[136:137]
	s_add_i32 m0, s54, 0x2000
	s_nop 0
	global_load_lds_dwordx4 v[144:145], off
	v_lshl_add_u64 v[144:145], s[50:51], 0, v[132:133]
	s_mov_b32 m0, s61
	s_nop 0
	global_load_lds_dwordx4 v[144:145], off
	v_lshl_add_u64 v[144:145], s[50:51], 0, v[134:135]
	s_mov_b32 m0, s62
	s_nop 0
	global_load_lds_dwordx4 v[144:145], off
	s_waitcnt vmcnt(8)
	s_waitcnt lgkmcnt(0)
	s_barrier
	s_setprio 3
	s_waitcnt lgkmcnt(0)
	v_mfma_f32_16x16x32_bf16 v[50:53], v[148:151], v[198:201], v[50:53]
	v_mfma_f32_16x16x32_bf16 v[62:65], v[158:161], v[198:201], v[62:65]
	v_mfma_f32_16x16x32_bf16 v[34:37], v[148:151], v[206:209], v[34:37]
	v_mfma_f32_16x16x32_bf16 v[38:41], v[158:161], v[206:209], v[38:41]
	v_mfma_f32_16x16x32_bf16 v[18:21], v[148:151], v[214:217], v[18:21]
	v_mfma_f32_16x16x32_bf16 v[26:29], v[158:161], v[214:217], v[26:29]
	v_mfma_f32_16x16x32_bf16 v[2:5], v[148:151], v[222:225], v[2:5]
	v_mfma_f32_16x16x32_bf16 v[6:9], v[158:161], v[222:225], v[6:9]
	v_mfma_f32_16x16x32_bf16 v[50:53], v[152:155], v[202:205], v[50:53]
	v_mfma_f32_16x16x32_bf16 v[62:65], v[166:169], v[202:205], v[62:65]
	v_mfma_f32_16x16x32_bf16 v[34:37], v[152:155], v[210:213], v[34:37]
	v_mfma_f32_16x16x32_bf16 v[38:41], v[166:169], v[210:213], v[38:41]
	v_mfma_f32_16x16x32_bf16 v[18:21], v[152:155], v[218:221], v[18:21]
	v_mfma_f32_16x16x32_bf16 v[26:29], v[166:169], v[218:221], v[26:29]
	v_mfma_f32_16x16x32_bf16 v[2:5], v[152:155], v[226:229], v[2:5]
	v_mfma_f32_16x16x32_bf16 v[6:9], v[166:169], v[226:229], v[6:9]
	s_setprio 0
	s_setprio 3
	v_mfma_f32_16x16x32_bf16 v[54:57], v[170:173], v[198:201], v[54:57]
	v_mfma_f32_16x16x32_bf16 v[66:69], v[178:181], v[198:201], v[66:69]
	v_mfma_f32_16x16x32_bf16 v[42:45], v[170:173], v[206:209], v[42:45]
	v_mfma_f32_16x16x32_bf16 v[46:49], v[178:181], v[206:209], v[46:49]
	v_mfma_f32_16x16x32_bf16 v[22:25], v[170:173], v[214:217], v[22:25]
	v_mfma_f32_16x16x32_bf16 v[30:33], v[178:181], v[214:217], v[30:33]
	v_mfma_f32_16x16x32_bf16 v[10:13], v[170:173], v[222:225], v[10:13]
	v_mfma_f32_16x16x32_bf16 v[14:17], v[178:181], v[222:225], v[14:17]
	v_mfma_f32_16x16x32_bf16 v[54:57], v[174:177], v[202:205], v[54:57]
	v_mfma_f32_16x16x32_bf16 v[66:69], v[194:197], v[202:205], v[66:69]
	v_mfma_f32_16x16x32_bf16 v[42:45], v[174:177], v[210:213], v[42:45]
	v_mfma_f32_16x16x32_bf16 v[46:49], v[194:197], v[210:213], v[46:49]
	v_mfma_f32_16x16x32_bf16 v[22:25], v[174:177], v[218:221], v[22:25]
	v_mfma_f32_16x16x32_bf16 v[30:33], v[194:197], v[218:221], v[30:33]
	v_mfma_f32_16x16x32_bf16 v[10:13], v[174:177], v[226:229], v[10:13]
	v_mfma_f32_16x16x32_bf16 v[14:17], v[194:197], v[226:229], v[14:17]
	s_setprio 0
	s_barrier
	s_add_i32 s66, s66, 2
	s_add_u32 s52, s52, 0x10000
	s_addc_u32 s53, s53, 0
	s_add_u32 s49, s49, 0x10000
	s_addc_u32 s65, s65, 0
	s_cmpk_gt_u32 s66, 0x7d
	s_cbranch_scc0 .LBB0_1334
	s_and_b64 vcc, exec, s[10:11]
	s_cbranch_vccz .LBB0_1337
	s_barrier

.LBB0_1376:
	s_add_u32 s16, s44, 0x4000
	s_addc_u32 s17, s45, 0
	s_cmpk_eq_i32 s60, 0x7c
	s_cselect_b32 s48, s56, s16
	s_cselect_b32 s49, s11, s17
	s_cselect_b32 s47, s1, s59
	s_cselect_b32 s46, s57, s58
	s_add_u32 s42, s48, 0x8000
	s_addc_u32 s43, s49, 0
	s_add_i32 s16, 0, 0x10000
	v_add_u32_e32 v147, s16, v144
	s_add_i32 s61, 0, 0x14000
	ds_read_b128 v[148:151], v147
	ds_read_b128 v[152:155], v147 offset:1024
	ds_read_b128 v[158:161], v147 offset:2048
	ds_read_b128 v[166:169], v147 offset:3072
	v_add_u32_e32 v147, s61, v144
	ds_read_b128 v[170:173], v147
	ds_read_b128 v[174:177], v147 offset:1024
	ds_read_b128 v[178:181], v147 offset:2048
	ds_read_b128 v[194:197], v147 offset:3072
	v_lshl_add_u64 v[182:183], s[44:45], 0, v[114:115]
	s_add_i32 m0, s37, 0xc000
	ds_read_b128 v[198:201], v146
	ds_read_b128 v[202:205], v146 offset:1024
	ds_read_b128 v[206:209], v146 offset:2048
	ds_read_b128 v[210:213], v146 offset:3072
	ds_read_b128 v[214:217], v146 offset:4096
	ds_read_b128 v[218:221], v146 offset:5120
	ds_read_b128 v[222:225], v146 offset:6144
	ds_read_b128 v[226:229], v146 offset:7168
	global_load_lds_dwordx4 v[182:183], off
	v_lshl_add_u64 v[182:183], s[44:45], 0, v[142:143]
	s_add_i32 m0, s37, 0xe000
	s_nop 0
	global_load_lds_dwordx4 v[182:183], off
	s_waitcnt vmcnt(8)
	s_waitcnt lgkmcnt(0)
	s_barrier
	s_setprio 3
	s_waitcnt lgkmcnt(0)
	v_mfma_f32_16x16x32_bf16 v[2:5], v[148:151], v[198:201], v[2:5]
	v_mfma_f32_16x16x32_bf16 v[6:9], v[158:161], v[198:201], v[6:9]
	v_mfma_f32_16x16x32_bf16 v[10:13], v[148:151], v[206:209], v[10:13]
	v_mfma_f32_16x16x32_bf16 v[14:17], v[158:161], v[206:209], v[14:17]
	v_mfma_f32_16x16x32_bf16 v[26:29], v[148:151], v[214:217], v[26:29]
	v_mfma_f32_16x16x32_bf16 v[30:33], v[158:161], v[214:217], v[30:33]
	v_mfma_f32_16x16x32_bf16 v[42:45], v[148:151], v[222:225], v[42:45]
	v_mfma_f32_16x16x32_bf16 v[46:49], v[158:161], v[222:225], v[46:49]
	v_mfma_f32_16x16x32_bf16 v[2:5], v[152:155], v[202:205], v[2:5]
	v_mfma_f32_16x16x32_bf16 v[6:9], v[166:169], v[202:205], v[6:9]
	v_mfma_f32_16x16x32_bf16 v[10:13], v[152:155], v[210:213], v[10:13]
	v_mfma_f32_16x16x32_bf16 v[14:17], v[166:169], v[210:213], v[14:17]
	v_mfma_f32_16x16x32_bf16 v[26:29], v[152:155], v[218:221], v[26:29]
	v_mfma_f32_16x16x32_bf16 v[30:33], v[166:169], v[218:221], v[30:33]
	v_mfma_f32_16x16x32_bf16 v[42:45], v[152:155], v[226:229], v[42:45]
	v_mfma_f32_16x16x32_bf16 v[46:49], v[166:169], v[226:229], v[46:49]
	s_setprio 0
	s_setprio 3
	v_mfma_f32_16x16x32_bf16 v[18:21], v[170:173], v[198:201], v[18:21]
	v_mfma_f32_16x16x32_bf16 v[22:25], v[178:181], v[198:201], v[22:25]
	v_mfma_f32_16x16x32_bf16 v[34:37], v[170:173], v[206:209], v[34:37]
	v_mfma_f32_16x16x32_bf16 v[38:41], v[178:181], v[206:209], v[38:41]
	v_mfma_f32_16x16x32_bf16 v[50:53], v[170:173], v[214:217], v[50:53]
	v_mfma_f32_16x16x32_bf16 v[54:57], v[178:181], v[214:217], v[54:57]
	v_mfma_f32_16x16x32_bf16 v[58:61], v[170:173], v[222:225], v[58:61]
	v_mfma_f32_16x16x32_bf16 v[62:65], v[178:181], v[222:225], v[62:65]
	v_mfma_f32_16x16x32_bf16 v[18:21], v[174:177], v[202:205], v[18:21]
	v_mfma_f32_16x16x32_bf16 v[22:25], v[194:197], v[202:205], v[22:25]
	v_mfma_f32_16x16x32_bf16 v[34:37], v[174:177], v[210:213], v[34:37]
	v_mfma_f32_16x16x32_bf16 v[38:41], v[194:197], v[210:213], v[38:41]
	v_mfma_f32_16x16x32_bf16 v[50:53], v[174:177], v[218:221], v[50:53]
	v_mfma_f32_16x16x32_bf16 v[54:57], v[194:197], v[218:221], v[54:57]
	v_mfma_f32_16x16x32_bf16 v[58:61], v[174:177], v[226:229], v[58:61]
	v_mfma_f32_16x16x32_bf16 v[62:65], v[194:197], v[226:229], v[62:65]
	s_setprio 0
	s_barrier
	s_add_i32 s16, s16, s24
	v_lshl_add_u64 v[182:183], s[46:47], 0, v[134:135]
	s_mov_b32 m0, s16
	ds_read_b128 v[198:201], v146 offset:16384
	ds_read_b128 v[202:205], v146 offset:17408
	ds_read_b128 v[206:209], v146 offset:18432
	ds_read_b128 v[210:213], v146 offset:19456
	ds_read_b128 v[214:217], v146 offset:20480
	ds_read_b128 v[218:221], v146 offset:21504
	ds_read_b128 v[222:225], v146 offset:22528
	ds_read_b128 v[226:229], v146 offset:23552
	global_load_lds_dwordx4 v[182:183], off
	s_add_i32 m0, s16, 0x2000
	s_add_u32 s16, s46, 0x1000
	v_lshl_add_u64 v[182:183], s[46:47], 0, v[138:139]
	s_addc_u32 s17, s47, 0
	s_add_i32 s61, s61, s24
	global_load_lds_dwordx4 v[182:183], off
	v_lshl_add_u64 v[182:183], s[16:17], 0, v[134:135]
	s_mov_b32 m0, s61
	s_nop 0
	global_load_lds_dwordx4 v[182:183], off
	v_lshl_add_u64 v[182:183], s[16:17], 0, v[138:139]
	s_add_i32 m0, s61, 0x2000
	s_nop 0
	global_load_lds_dwordx4 v[182:183], off
	v_lshl_add_u64 v[182:183], s[48:49], 0, v[132:133]
	s_mov_b32 m0, s37
	s_nop 0
	global_load_lds_dwordx4 v[182:183], off
	v_lshl_add_u64 v[182:183], s[48:49], 0, v[136:137]
	s_mov_b32 m0, s50
	s_nop 0
	global_load_lds_dwordx4 v[182:183], off
	s_waitcnt vmcnt(8)
	s_waitcnt lgkmcnt(0)
	s_barrier
	s_setprio 3
	s_waitcnt lgkmcnt(0)
	v_mfma_f32_16x16x32_bf16 v[66:69], v[148:151], v[198:201], v[66:69]
	v_mfma_f32_16x16x32_bf16 v[70:73], v[158:161], v[198:201], v[70:73]
	v_mfma_f32_16x16x32_bf16 v[74:77], v[148:151], v[206:209], v[74:77]
	v_mfma_f32_16x16x32_bf16 v[78:81], v[158:161], v[206:209], v[78:81]
	v_mfma_f32_16x16x32_bf16 v[86:89], v[148:151], v[214:217], v[86:89]
	v_mfma_f32_16x16x32_bf16 v[94:97], v[158:161], v[214:217], v[94:97]
	v_mfma_f32_16x16x32_bf16 v[102:105], v[148:151], v[222:225], v[102:105]
	v_mfma_f32_16x16x32_bf16 v[110:113], v[158:161], v[222:225], v[110:113]
	v_mfma_f32_16x16x32_bf16 v[66:69], v[152:155], v[202:205], v[66:69]
	v_mfma_f32_16x16x32_bf16 v[70:73], v[166:169], v[202:205], v[70:73]
	v_mfma_f32_16x16x32_bf16 v[74:77], v[152:155], v[210:213], v[74:77]
	v_mfma_f32_16x16x32_bf16 v[78:81], v[166:169], v[210:213], v[78:81]
	v_mfma_f32_16x16x32_bf16 v[86:89], v[152:155], v[218:221], v[86:89]
	v_mfma_f32_16x16x32_bf16 v[94:97], v[166:169], v[218:221], v[94:97]
	v_mfma_f32_16x16x32_bf16 v[102:105], v[152:155], v[226:229], v[102:105]
	v_mfma_f32_16x16x32_bf16 v[110:113], v[166:169], v[226:229], v[110:113]
	s_setprio 0
	s_setprio 3
	v_mfma_f32_16x16x32_bf16 v[82:85], v[170:173], v[198:201], v[82:85]
	v_mfma_f32_16x16x32_bf16 v[90:93], v[178:181], v[198:201], v[90:93]
	v_mfma_f32_16x16x32_bf16 v[98:101], v[170:173], v[206:209], v[98:101]
	v_mfma_f32_16x16x32_bf16 v[106:109], v[178:181], v[206:209], v[106:109]
	v_mfma_f32_16x16x32_bf16 v[116:119], v[170:173], v[214:217], v[116:119]
	v_mfma_f32_16x16x32_bf16 v[120:123], v[178:181], v[214:217], v[120:123]
	v_mfma_f32_16x16x32_bf16 v[124:127], v[170:173], v[222:225], v[124:127]
	v_mfma_f32_16x16x32_bf16 v[128:131], v[178:181], v[222:225], v[128:131]
	v_mfma_f32_16x16x32_bf16 v[82:85], v[174:177], v[202:205], v[82:85]
	v_mfma_f32_16x16x32_bf16 v[90:93], v[194:197], v[202:205], v[90:93]
	v_mfma_f32_16x16x32_bf16 v[98:101], v[174:177], v[210:213], v[98:101]
	v_mfma_f32_16x16x32_bf16 v[106:109], v[194:197], v[210:213], v[106:109]
	v_mfma_f32_16x16x32_bf16 v[116:119], v[174:177], v[218:221], v[116:119]
	v_mfma_f32_16x16x32_bf16 v[120:123], v[194:197], v[218:221], v[120:123]
	v_mfma_f32_16x16x32_bf16 v[124:127], v[174:177], v[226:229], v[124:127]
	v_mfma_f32_16x16x32_bf16 v[128:131], v[194:197], v[226:229], v[128:131]
	s_setprio 0
	s_barrier
	s_add_i32 s61, 0, 0x18000
	v_add_u32_e32 v147, s61, v144
	s_add_i32 s62, 0, 0x1c000
	ds_read_b128 v[148:151], v147
	ds_read_b128 v[152:155], v147 offset:1024
	ds_read_b128 v[158:161], v147 offset:2048
	ds_read_b128 v[166:169], v147 offset:3072
	v_add_u32_e32 v147, s62, v144
	ds_read_b128 v[170:173], v147
	ds_read_b128 v[174:177], v147 offset:1024
	ds_read_b128 v[178:181], v147 offset:2048
	ds_read_b128 v[194:197], v147 offset:3072
	s_add_u32 s16, s48, 0x4000
	s_addc_u32 s17, s49, 0
	s_mov_b32 m0, s51
	v_lshl_add_u64 v[182:183], s[16:17], 0, v[132:133]
	ds_read_b128 v[198:201], v146 offset:32768
	ds_read_b128 v[202:205], v146 offset:33792
	ds_read_b128 v[206:209], v146 offset:34816
	ds_read_b128 v[210:213], v146 offset:35840
	ds_read_b128 v[214:217], v146 offset:36864
	ds_read_b128 v[218:221], v146 offset:37888
	ds_read_b128 v[222:225], v146 offset:38912
	ds_read_b128 v[226:229], v146 offset:39936
	global_load_lds_dwordx4 v[182:183], off
	v_lshl_add_u64 v[182:183], s[16:17], 0, v[136:137]
	s_mov_b32 m0, s52
	s_nop 0
	global_load_lds_dwordx4 v[182:183], off
	s_waitcnt vmcnt(8)
	s_waitcnt lgkmcnt(0)
	s_barrier
	s_setprio 3
	s_waitcnt lgkmcnt(0)
	v_mfma_f32_16x16x32_bf16 v[2:5], v[148:151], v[198:201], v[2:5]
	v_mfma_f32_16x16x32_bf16 v[6:9], v[158:161], v[198:201], v[6:9]
	v_mfma_f32_16x16x32_bf16 v[10:13], v[148:151], v[206:209], v[10:13]
	v_mfma_f32_16x16x32_bf16 v[14:17], v[158:161], v[206:209], v[14:17]
	v_mfma_f32_16x16x32_bf16 v[26:29], v[148:151], v[214:217], v[26:29]
	v_mfma_f32_16x16x32_bf16 v[30:33], v[158:161], v[214:217], v[30:33]
	v_mfma_f32_16x16x32_bf16 v[42:45], v[148:151], v[222:225], v[42:45]
	v_mfma_f32_16x16x32_bf16 v[46:49], v[158:161], v[222:225], v[46:49]
	v_mfma_f32_16x16x32_bf16 v[2:5], v[152:155], v[202:205], v[2:5]
	v_mfma_f32_16x16x32_bf16 v[6:9], v[166:169], v[202:205], v[6:9]
	v_mfma_f32_16x16x32_bf16 v[10:13], v[152:155], v[210:213], v[10:13]
	v_mfma_f32_16x16x32_bf16 v[14:17], v[166:169], v[210:213], v[14:17]
	v_mfma_f32_16x16x32_bf16 v[26:29], v[152:155], v[218:221], v[26:29]
	v_mfma_f32_16x16x32_bf16 v[30:33], v[166:169], v[218:221], v[30:33]
	v_mfma_f32_16x16x32_bf16 v[42:45], v[152:155], v[226:229], v[42:45]
	v_mfma_f32_16x16x32_bf16 v[46:49], v[166:169], v[226:229], v[46:49]
	s_setprio 0
	s_setprio 3
	v_mfma_f32_16x16x32_bf16 v[18:21], v[170:173], v[198:201], v[18:21]
	v_mfma_f32_16x16x32_bf16 v[22:25], v[178:181], v[198:201], v[22:25]
	v_mfma_f32_16x16x32_bf16 v[34:37], v[170:173], v[206:209], v[34:37]
	v_mfma_f32_16x16x32_bf16 v[38:41], v[178:181], v[206:209], v[38:41]
	v_mfma_f32_16x16x32_bf16 v[50:53], v[170:173], v[214:217], v[50:53]
	v_mfma_f32_16x16x32_bf16 v[54:57], v[178:181], v[214:217], v[54:57]
	v_mfma_f32_16x16x32_bf16 v[58:61], v[170:173], v[222:225], v[58:61]
	v_mfma_f32_16x16x32_bf16 v[62:65], v[178:181], v[222:225], v[62:65]
	v_mfma_f32_16x16x32_bf16 v[18:21], v[174:177], v[202:205], v[18:21]
	v_mfma_f32_16x16x32_bf16 v[22:25], v[194:197], v[202:205], v[22:25]
	v_mfma_f32_16x16x32_bf16 v[34:37], v[174:177], v[210:213], v[34:37]
	v_mfma_f32_16x16x32_bf16 v[38:41], v[194:197], v[210:213], v[38:41]
	v_mfma_f32_16x16x32_bf16 v[50:53], v[174:177], v[218:221], v[50:53]
	v_mfma_f32_16x16x32_bf16 v[54:57], v[194:197], v[218:221], v[54:57]
	v_mfma_f32_16x16x32_bf16 v[58:61], v[174:177], v[226:229], v[58:61]
	v_mfma_f32_16x16x32_bf16 v[62:65], v[194:197], v[226:229], v[62:65]
	s_setprio 0
	s_barrier
	s_add_u32 s16, s46, 0x8000
	s_addc_u32 s17, s47, 0
	s_add_i32 s48, s61, s24
	v_lshl_add_u64 v[182:183], s[16:17], 0, v[134:135]
	s_mov_b32 m0, s48
	ds_read_b128 v[198:201], v146 offset:49152
	ds_read_b128 v[202:205], v146 offset:50176
	ds_read_b128 v[206:209], v146 offset:51200
	ds_read_b128 v[210:213], v146 offset:52224
	ds_read_b128 v[214:217], v146 offset:53248
	ds_read_b128 v[218:221], v146 offset:54272
	ds_read_b128 v[222:225], v146 offset:55296
	ds_read_b128 v[226:229], v146 offset:56320
	global_load_lds_dwordx4 v[182:183], off
	s_add_i32 m0, s48, 0x2000
	v_lshl_add_u64 v[182:183], s[16:17], 0, v[138:139]
	s_add_u32 s16, s46, 0x9000
	s_addc_u32 s17, s47, 0
	s_add_i32 s46, s62, s24
	global_load_lds_dwordx4 v[182:183], off
	v_lshl_add_u64 v[182:183], s[16:17], 0, v[134:135]
	s_mov_b32 m0, s46
	s_nop 0
	global_load_lds_dwordx4 v[182:183], off
	v_lshl_add_u64 v[182:183], s[16:17], 0, v[138:139]
	s_add_i32 m0, s46, 0x2000
	s_nop 0
	global_load_lds_dwordx4 v[182:183], off
	v_lshl_add_u64 v[182:183], s[42:43], 0, v[132:133]
	s_mov_b32 m0, s53
	s_nop 0
	global_load_lds_dwordx4 v[182:183], off
	v_lshl_add_u64 v[182:183], s[42:43], 0, v[136:137]
	s_mov_b32 m0, s54
	s_nop 0
	global_load_lds_dwordx4 v[182:183], off
	s_waitcnt vmcnt(8)
	s_waitcnt lgkmcnt(0)
	s_barrier
	s_setprio 3
	s_waitcnt lgkmcnt(0)
	v_mfma_f32_16x16x32_bf16 v[66:69], v[148:151], v[198:201], v[66:69]
	v_mfma_f32_16x16x32_bf16 v[70:73], v[158:161], v[198:201], v[70:73]
	v_mfma_f32_16x16x32_bf16 v[74:77], v[148:151], v[206:209], v[74:77]
	v_mfma_f32_16x16x32_bf16 v[78:81], v[158:161], v[206:209], v[78:81]
	v_mfma_f32_16x16x32_bf16 v[86:89], v[148:151], v[214:217], v[86:89]
	v_mfma_f32_16x16x32_bf16 v[94:97], v[158:161], v[214:217], v[94:97]
	v_mfma_f32_16x16x32_bf16 v[102:105], v[148:151], v[222:225], v[102:105]
	v_mfma_f32_16x16x32_bf16 v[110:113], v[158:161], v[222:225], v[110:113]
	v_mfma_f32_16x16x32_bf16 v[66:69], v[152:155], v[202:205], v[66:69]
	v_mfma_f32_16x16x32_bf16 v[70:73], v[166:169], v[202:205], v[70:73]
	v_mfma_f32_16x16x32_bf16 v[74:77], v[152:155], v[210:213], v[74:77]
	v_mfma_f32_16x16x32_bf16 v[78:81], v[166:169], v[210:213], v[78:81]
	v_mfma_f32_16x16x32_bf16 v[86:89], v[152:155], v[218:221], v[86:89]
	v_mfma_f32_16x16x32_bf16 v[94:97], v[166:169], v[218:221], v[94:97]
	v_mfma_f32_16x16x32_bf16 v[102:105], v[152:155], v[226:229], v[102:105]
	v_mfma_f32_16x16x32_bf16 v[110:113], v[166:169], v[226:229], v[110:113]
	s_setprio 0
	s_setprio 3
	v_mfma_f32_16x16x32_bf16 v[82:85], v[170:173], v[198:201], v[82:85]
	v_mfma_f32_16x16x32_bf16 v[90:93], v[178:181], v[198:201], v[90:93]
	v_mfma_f32_16x16x32_bf16 v[98:101], v[170:173], v[206:209], v[98:101]
	v_mfma_f32_16x16x32_bf16 v[106:109], v[178:181], v[206:209], v[106:109]
	v_mfma_f32_16x16x32_bf16 v[116:119], v[170:173], v[214:217], v[116:119]
	v_mfma_f32_16x16x32_bf16 v[120:123], v[178:181], v[214:217], v[120:123]
	v_mfma_f32_16x16x32_bf16 v[124:127], v[170:173], v[222:225], v[124:127]
	v_mfma_f32_16x16x32_bf16 v[128:131], v[178:181], v[222:225], v[128:131]
	v_mfma_f32_16x16x32_bf16 v[82:85], v[174:177], v[202:205], v[82:85]
	v_mfma_f32_16x16x32_bf16 v[90:93], v[194:197], v[202:205], v[90:93]
	v_mfma_f32_16x16x32_bf16 v[98:101], v[174:177], v[210:213], v[98:101]
	v_mfma_f32_16x16x32_bf16 v[106:109], v[194:197], v[210:213], v[106:109]
	v_mfma_f32_16x16x32_bf16 v[116:119], v[174:177], v[218:221], v[116:119]
	v_mfma_f32_16x16x32_bf16 v[120:123], v[194:197], v[218:221], v[120:123]
	v_mfma_f32_16x16x32_bf16 v[124:127], v[174:177], v[226:229], v[124:127]
	v_mfma_f32_16x16x32_bf16 v[128:131], v[194:197], v[226:229], v[128:131]
	s_setprio 0
	s_barrier
	s_add_i32 s60, s60, 2
	s_add_u32 s44, s44, 0x10000
	s_addc_u32 s45, s45, 0
	s_add_u32 s58, s58, 0x10000
	s_addc_u32 s59, s59, 0
	s_cmpk_gt_u32 s60, 0x7d
	s_cbranch_scc0 .LBB0_1376
	s_and_b64 vcc, exec, s[8:9]
	s_cbranch_vccz .LBB0_1379
	s_barrier
